# MoE down epilogue: the 16 fp8 8-byte stores per lane become 8 16-byte stores via v_permlane16_swap (section 7.3), plain cache policy
# speedup vs baseline: 1.0043x; 1.0043x over previous
.LBB0_916:
	v_mul_f32_e32 v6, 0x3b800000, v152
	v_med3_f32 v8, v6, s72, v204
	v_mul_f32_e32 v6, 0x3b800000, v157
	v_med3_f32 v7, v6, s72, v204
	v_mul_f32_e32 v6, 0x3b800000, v153
	v_lshl_add_u32 v4, s26, 8, v184
	v_med3_f32 v9, v6, s72, v204
	v_mul_f32_e32 v6, 0x3b800000, v158
	v_ashrrev_i32_e32 v5, 31, v4
	v_med3_f32 v10, v6, s72, v204
	v_mul_f32_e32 v6, 0x3b800000, v154
	v_lshlrev_b64 v[0:1], 10, v[4:5]
	v_mul_f32_e32 v5, 0x3b800000, v156
	v_med3_f32 v11, v6, s72, v204
	v_mul_f32_e32 v6, 0x3b800000, v159
	v_med3_f32 v5, v5, s72, v204
	v_med3_f32 v12, v6, s72, v204
	v_mov_b32_e32 v6, 0
	v_cvt_pk_fp8_f32 v6, v5, v7
	v_mov_b32_e32 v7, 0
	v_cvt_pk_fp8_f32 v7, v8, v9
	v_mul_f32_e32 v8, 0x3b800000, v144
	v_mul_f32_e32 v5, 0x3b800000, v155
	v_cvt_pk_fp8_f32 v6, v10, v12 op_sel:[0,0,1]
	v_med3_f32 v10, v8, s72, v204
	v_mul_f32_e32 v8, 0x3b800000, v149
	v_med3_f32 v5, v5, s72, v204
	v_med3_f32 v9, v8, s72, v204
	v_mul_f32_e32 v8, 0x3b800000, v145
	v_cvt_pk_fp8_f32 v7, v11, v5 op_sel:[0,0,1]
	v_med3_f32 v11, v8, s72, v204
	v_mul_f32_e32 v8, 0x3b800000, v150
	v_med3_f32 v12, v8, s72, v204
	v_mul_f32_e32 v8, 0x3b800000, v146
	v_mul_f32_e32 v5, 0x3b800000, v148
	v_med3_f32 v13, v8, s72, v204
	v_mul_f32_e32 v8, 0x3b800000, v151
	v_med3_f32 v5, v5, s72, v204
	v_med3_f32 v14, v8, s72, v204
	v_mov_b32_e32 v8, 0
	v_cvt_pk_fp8_f32 v8, v5, v9
	v_mov_b32_e32 v9, 0
	v_cvt_pk_fp8_f32 v9, v10, v11
	v_mul_f32_e32 v5, 0x3b800000, v147
	v_med3_f32 v5, v5, s72, v204
	v_readlane_b32 s34, v254, 50
	v_lshl_or_b32 v2, s73, 8, v201
	v_cvt_pk_fp8_f32 v8, v12, v14 op_sel:[0,0,1]
	v_cvt_pk_fp8_f32 v9, v13, v5 op_sel:[0,0,1]
	v_readlane_b32 s35, v254, 51
	v_ashrrev_i32_e32 v3, 31, v2
	v_mul_f32_e32 v5, 0x3b800000, v140
	v_lshl_add_u64 v[0:1], s[34:35], 0, v[0:1]
	v_lshl_add_u64 v[0:1], v[0:1], 0, v[2:3]
	s_mov_b32 s98, 0xffff0000
	s_mov_b32 s99, 0xffff0000
	v_mov_b32_e32 v178, 0x78
	v_mov_b32_e32 v179, 0
	v_permlane16_swap_b32_e32 v6, v8
	v_permlane16_swap_b32_e32 v7, v9
	v_cndmask_b32_e64 v178, 0, v178, s[98:99]
	v_cndmask_b32_e64 v176, v0, v0, s[98:99]
	v_cndmask_b32_e64 v177, v1, v1, s[98:99]
	v_lshl_add_u64 v[176:177], v[176:177], 0, v[178:179]
	global_store_dwordx4 v[176:177], v[6:9], off
	s_nop 1
	v_mul_f32_e32 v8, 0x3b800000, v136
	v_med3_f32 v10, v8, s72, v204
	v_mul_f32_e32 v8, 0x3b800000, v141
	v_med3_f32 v9, v8, s72, v204
	v_mul_f32_e32 v8, 0x3b800000, v137
	v_med3_f32 v11, v8, s72, v204
	v_mul_f32_e32 v8, 0x3b800000, v142
	v_med3_f32 v12, v8, s72, v204
	v_mul_f32_e32 v8, 0x3b800000, v138
	v_med3_f32 v13, v8, s72, v204
	v_mul_f32_e32 v8, 0x3b800000, v143
	v_med3_f32 v5, v5, s72, v204
	v_med3_f32 v14, v8, s72, v204
	v_mov_b32_e32 v8, 0
	v_cvt_pk_fp8_f32 v8, v5, v9
	v_mov_b32_e32 v9, 0
	v_cvt_pk_fp8_f32 v9, v10, v11
	v_mul_f32_e32 v10, 0x3b800000, v128
	v_mul_f32_e32 v5, 0x3b800000, v139
	v_cvt_pk_fp8_f32 v8, v12, v14 op_sel:[0,0,1]
	v_med3_f32 v12, v10, s72, v204
	v_mul_f32_e32 v10, 0x3b800000, v133
	v_med3_f32 v5, v5, s72, v204
	v_med3_f32 v11, v10, s72, v204
	v_mul_f32_e32 v10, 0x3b800000, v129
	v_cvt_pk_fp8_f32 v9, v13, v5 op_sel:[0,0,1]
	v_med3_f32 v13, v10, s72, v204
	v_mul_f32_e32 v10, 0x3b800000, v134
	v_med3_f32 v14, v10, s72, v204
	v_mul_f32_e32 v10, 0x3b800000, v130
	v_mul_f32_e32 v5, 0x3b800000, v132
	v_med3_f32 v15, v10, s72, v204
	v_mul_f32_e32 v10, 0x3b800000, v135
	v_med3_f32 v5, v5, s72, v204
	v_med3_f32 v16, v10, s72, v204
	v_mov_b32_e32 v10, 0
	v_cvt_pk_fp8_f32 v10, v5, v11
	v_mov_b32_e32 v11, 0
	v_cvt_pk_fp8_f32 v11, v12, v13
	v_or_b32_e32 v6, 16, v4
	v_mul_f32_e32 v5, 0x3b800000, v131
	v_ashrrev_i32_e32 v7, 31, v6
	v_med3_f32 v5, v5, s72, v204
	v_lshlrev_b64 v[6:7], 10, v[6:7]
	v_cvt_pk_fp8_f32 v10, v14, v16 op_sel:[0,0,1]
	v_cvt_pk_fp8_f32 v11, v15, v5 op_sel:[0,0,1]
	v_lshl_add_u64 v[6:7], s[34:35], 0, v[6:7]
	v_lshl_add_u64 v[6:7], v[6:7], 0, v[2:3]
	s_mov_b32 s98, 0xffff0000
	s_mov_b32 s99, 0xffff0000
	v_mov_b32_e32 v178, 0x78
	v_mov_b32_e32 v179, 0
	v_permlane16_swap_b32_e32 v8, v10
	v_permlane16_swap_b32_e32 v9, v11
	v_cndmask_b32_e64 v178, 0, v178, s[98:99]
	v_cndmask_b32_e64 v176, v6, v6, s[98:99]
	v_cndmask_b32_e64 v177, v7, v7, s[98:99]
	v_lshl_add_u64 v[176:177], v[176:177], 0, v[178:179]
	global_store_dwordx4 v[176:177], v[8:11], off
	s_nop 1
	v_mul_f32_e32 v8, 0x3b800000, v120
	v_med3_f32 v10, v8, s72, v204
	v_mul_f32_e32 v8, 0x3b800000, v125
	v_med3_f32 v9, v8, s72, v204
	v_mul_f32_e32 v8, 0x3b800000, v121
	v_med3_f32 v11, v8, s72, v204
	v_mul_f32_e32 v8, 0x3b800000, v126
	v_med3_f32 v12, v8, s72, v204
	v_mul_f32_e32 v8, 0x3b800000, v122
	v_mul_f32_e32 v5, 0x3b800000, v124
	v_med3_f32 v13, v8, s72, v204
	v_mul_f32_e32 v8, 0x3b800000, v127
	v_med3_f32 v5, v5, s72, v204
	v_med3_f32 v14, v8, s72, v204
	v_mov_b32_e32 v8, 0
	v_cvt_pk_fp8_f32 v8, v5, v9
	v_mov_b32_e32 v9, 0
	v_cvt_pk_fp8_f32 v9, v10, v11
	v_mul_f32_e32 v10, 0x3b800000, v112
	v_mul_f32_e32 v5, 0x3b800000, v123
	v_cvt_pk_fp8_f32 v8, v12, v14 op_sel:[0,0,1]
	v_med3_f32 v12, v10, s72, v204
	v_mul_f32_e32 v10, 0x3b800000, v117
	v_med3_f32 v5, v5, s72, v204
	v_med3_f32 v11, v10, s72, v204
	v_mul_f32_e32 v10, 0x3b800000, v113
	v_cvt_pk_fp8_f32 v9, v13, v5 op_sel:[0,0,1]
	v_med3_f32 v13, v10, s72, v204
	v_mul_f32_e32 v10, 0x3b800000, v118
	v_med3_f32 v14, v10, s72, v204
	v_mul_f32_e32 v10, 0x3b800000, v114
	v_mul_f32_e32 v5, 0x3b800000, v116
	v_med3_f32 v15, v10, s72, v204
	v_mul_f32_e32 v10, 0x3b800000, v119
	v_med3_f32 v5, v5, s72, v204
	v_med3_f32 v16, v10, s72, v204
	v_mov_b32_e32 v10, 0
	v_cvt_pk_fp8_f32 v10, v5, v11
	v_mov_b32_e32 v11, 0
	v_cvt_pk_fp8_f32 v11, v12, v13
	v_or_b32_e32 v6, 32, v4
	v_mul_f32_e32 v5, 0x3b800000, v115
	v_ashrrev_i32_e32 v7, 31, v6
	v_med3_f32 v5, v5, s72, v204
	v_lshlrev_b64 v[6:7], 10, v[6:7]
	v_cvt_pk_fp8_f32 v10, v14, v16 op_sel:[0,0,1]
	v_cvt_pk_fp8_f32 v11, v15, v5 op_sel:[0,0,1]
	v_lshl_add_u64 v[6:7], s[34:35], 0, v[6:7]
	v_lshl_add_u64 v[6:7], v[6:7], 0, v[2:3]
	s_mov_b32 s98, 0xffff0000
	s_mov_b32 s99, 0xffff0000
	v_mov_b32_e32 v178, 0x78
	v_mov_b32_e32 v179, 0
	v_permlane16_swap_b32_e32 v8, v10
	v_permlane16_swap_b32_e32 v9, v11
	v_cndmask_b32_e64 v178, 0, v178, s[98:99]
	v_cndmask_b32_e64 v176, v6, v6, s[98:99]
	v_cndmask_b32_e64 v177, v7, v7, s[98:99]
	v_lshl_add_u64 v[176:177], v[176:177], 0, v[178:179]
	global_store_dwordx4 v[176:177], v[8:11], off
	s_nop 1
	v_mul_f32_e32 v6, 0x3b800000, v108
	v_med3_f32 v7, v6, s72, v204
	v_mul_f32_e32 v6, 0x3b800000, v104
	v_med3_f32 v8, v6, s72, v204
	v_mul_f32_e32 v6, 0x3b800000, v109
	v_med3_f32 v9, v6, s72, v204
	v_mul_f32_e32 v6, 0x3b800000, v105
	v_med3_f32 v10, v6, s72, v204
	v_mul_f32_e32 v6, 0x3b800000, v110
	v_med3_f32 v11, v6, s72, v204
	v_mul_f32_e32 v6, 0x3b800000, v106
	v_med3_f32 v12, v6, s72, v204
	v_mul_f32_e32 v6, 0x3b800000, v111
	v_med3_f32 v13, v6, s72, v204
	v_mov_b32_e32 v6, 0
	v_cvt_pk_fp8_f32 v6, v7, v9
	v_mov_b32_e32 v7, 0
	v_cvt_pk_fp8_f32 v7, v8, v10
	v_mul_f32_e32 v8, 0x3b800000, v107
	v_med3_f32 v8, v8, s72, v204
	v_cvt_pk_fp8_f32 v6, v11, v13 op_sel:[0,0,1]
	v_cvt_pk_fp8_f32 v7, v12, v8 op_sel:[0,0,1]
	v_mul_f32_e32 v8, 0x3b800000, v96
	v_med3_f32 v9, v8, s72, v204
	v_mul_f32_e32 v8, 0x3b800000, v88
	v_med3_f32 v10, v8, s72, v204
	v_mul_f32_e32 v8, 0x3b800000, v97
	v_med3_f32 v11, v8, s72, v204
	v_mul_f32_e32 v8, 0x3b800000, v89
	v_med3_f32 v12, v8, s72, v204
	v_mul_f32_e32 v8, 0x3b800000, v98
	v_med3_f32 v13, v8, s72, v204
	v_mul_f32_e32 v8, 0x3b800000, v90
	v_med3_f32 v14, v8, s72, v204
	v_mul_f32_e32 v8, 0x3b800000, v99
	v_med3_f32 v15, v8, s72, v204
	v_mov_b32_e32 v8, 0
	v_cvt_pk_fp8_f32 v8, v9, v11
	v_mov_b32_e32 v9, 0
	v_cvt_pk_fp8_f32 v9, v10, v12
	v_or_b32_e32 v4, 48, v4
	v_ashrrev_i32_e32 v5, 31, v4
	v_mul_f32_e32 v10, 0x3b800000, v91
	v_lshlrev_b64 v[4:5], 10, v[4:5]
	v_med3_f32 v10, v10, s72, v204
	v_cvt_pk_fp8_f32 v8, v13, v15 op_sel:[0,0,1]
	v_cvt_pk_fp8_f32 v9, v14, v10 op_sel:[0,0,1]
	v_lshl_add_u64 v[4:5], s[34:35], 0, v[4:5]
	v_lshl_add_u64 v[2:3], v[4:5], 0, v[2:3]
	v_mul_f32_e32 v4, 0x3b800000, v84
	v_med3_f32 v5, v4, s72, v204
	v_mul_f32_e32 v4, 0x3b800000, v76
	s_mov_b32 s98, 0xffff0000
	s_mov_b32 s99, 0xffff0000
	v_mov_b32_e32 v178, 0x78
	v_mov_b32_e32 v179, 0
	v_permlane16_swap_b32_e32 v6, v8
	v_permlane16_swap_b32_e32 v7, v9
	v_cndmask_b32_e64 v178, 0, v178, s[98:99]
	v_cndmask_b32_e64 v176, v2, v2, s[98:99]
	v_cndmask_b32_e64 v177, v3, v3, s[98:99]
	v_lshl_add_u64 v[176:177], v[176:177], 0, v[178:179]
	global_store_dwordx4 v[176:177], v[6:9], off
	s_nop 1
	v_med3_f32 v6, v4, s72, v204
	v_mul_f32_e32 v4, 0x3b800000, v85
	v_med3_f32 v7, v4, s72, v204
	v_mul_f32_e32 v4, 0x3b800000, v77
	v_med3_f32 v8, v4, s72, v204
	v_mul_f32_e32 v4, 0x3b800000, v86
	v_med3_f32 v9, v4, s72, v204
	v_mul_f32_e32 v4, 0x3b800000, v78
	v_med3_f32 v10, v4, s72, v204
	v_mul_f32_e32 v4, 0x3b800000, v87
	v_med3_f32 v11, v4, s72, v204
	v_mov_b32_e32 v4, 0
	v_cvt_pk_fp8_f32 v4, v5, v7
	v_mov_b32_e32 v5, 0
	v_cvt_pk_fp8_f32 v5, v6, v8
	v_mul_f32_e32 v6, 0x3b800000, v79
	v_med3_f32 v6, v6, s72, v204
	v_cvt_pk_fp8_f32 v4, v9, v11 op_sel:[0,0,1]
	v_cvt_pk_fp8_f32 v5, v10, v6 op_sel:[0,0,1]
	v_mul_f32_e32 v6, 0x3b800000, v100
	v_med3_f32 v7, v6, s72, v204
	v_mul_f32_e32 v6, 0x3b800000, v92
	v_med3_f32 v8, v6, s72, v204
	v_mul_f32_e32 v6, 0x3b800000, v101
	v_med3_f32 v9, v6, s72, v204
	v_mul_f32_e32 v6, 0x3b800000, v93
	v_med3_f32 v10, v6, s72, v204
	v_mul_f32_e32 v6, 0x3b800000, v102
	v_med3_f32 v11, v6, s72, v204
	v_mul_f32_e32 v6, 0x3b800000, v94
	v_med3_f32 v12, v6, s72, v204
	v_mul_f32_e32 v6, 0x3b800000, v103
	v_med3_f32 v13, v6, s72, v204
	v_mov_b32_e32 v6, 0
	v_cvt_pk_fp8_f32 v6, v7, v9
	v_mov_b32_e32 v7, 0
	v_cvt_pk_fp8_f32 v7, v8, v10
	v_mul_f32_e32 v8, 0x3b800000, v95
	v_med3_f32 v8, v8, s72, v204
	v_cvt_pk_fp8_f32 v6, v11, v13 op_sel:[0,0,1]
	v_cvt_pk_fp8_f32 v7, v12, v8 op_sel:[0,0,1]
	s_mov_b32 s25, 0x20000
	v_add_co_u32_e32 v8, vcc, s25, v0
	s_mov_b64 s[34:35], 0x20000
	s_nop 0
	v_addc_co_u32_e32 v9, vcc, 0, v1, vcc
	v_lshl_add_u64 v[2:3], v[0:1], 0, s[34:35]
	s_mov_b32 s98, 0xffff0000
	s_mov_b32 s99, 0xffff0000
	v_mov_b32_e32 v178, 0x78
	v_mov_b32_e32 v179, 0
	v_permlane16_swap_b32_e32 v4, v6
	v_permlane16_swap_b32_e32 v5, v7
	v_cndmask_b32_e64 v178, 0, v178, s[98:99]
	v_cndmask_b32_e64 v176, v8, v2, s[98:99]
	v_cndmask_b32_e64 v177, v9, v3, s[98:99]
	v_lshl_add_u64 v[176:177], v[176:177], 0, v[178:179]
	global_store_dwordx4 v[176:177], v[4:7], off
	s_nop 1
	v_mul_f32_e32 v4, 0x3b800000, v60
	v_med3_f32 v5, v4, s72, v204
	v_mul_f32_e32 v4, 0x3b800000, v48
	v_med3_f32 v6, v4, s72, v204
	v_mul_f32_e32 v4, 0x3b800000, v61
	v_med3_f32 v7, v4, s72, v204
	v_mul_f32_e32 v4, 0x3b800000, v49
	v_med3_f32 v8, v4, s72, v204
	v_mul_f32_e32 v4, 0x3b800000, v62
	v_med3_f32 v9, v4, s72, v204
	v_mul_f32_e32 v4, 0x3b800000, v50
	v_med3_f32 v10, v4, s72, v204
	v_mul_f32_e32 v4, 0x3b800000, v63
	v_med3_f32 v11, v4, s72, v204
	v_mov_b32_e32 v4, 0
	v_cvt_pk_fp8_f32 v4, v5, v7
	v_mov_b32_e32 v5, 0
	v_cvt_pk_fp8_f32 v5, v6, v8
	v_mul_f32_e32 v6, 0x3b800000, v51
	v_med3_f32 v6, v6, s72, v204
	v_cvt_pk_fp8_f32 v4, v9, v11 op_sel:[0,0,1]
	v_cvt_pk_fp8_f32 v5, v10, v6 op_sel:[0,0,1]
	v_mul_f32_e32 v6, 0x3b800000, v80
	v_med3_f32 v7, v6, s72, v204
	v_mul_f32_e32 v6, 0x3b800000, v72
	v_med3_f32 v8, v6, s72, v204
	v_mul_f32_e32 v6, 0x3b800000, v81
	v_med3_f32 v9, v6, s72, v204
	v_mul_f32_e32 v6, 0x3b800000, v73
	v_med3_f32 v10, v6, s72, v204
	v_mul_f32_e32 v6, 0x3b800000, v82
	v_med3_f32 v11, v6, s72, v204
	v_mul_f32_e32 v6, 0x3b800000, v74
	v_med3_f32 v12, v6, s72, v204
	v_mul_f32_e32 v6, 0x3b800000, v83
	v_med3_f32 v13, v6, s72, v204
	v_mov_b32_e32 v6, 0
	v_cvt_pk_fp8_f32 v6, v7, v9
	v_mov_b32_e32 v7, 0
	v_cvt_pk_fp8_f32 v7, v8, v10
	v_mul_f32_e32 v8, 0x3b800000, v75
	v_med3_f32 v8, v8, s72, v204
	v_cvt_pk_fp8_f32 v6, v11, v13 op_sel:[0,0,1]
	v_cvt_pk_fp8_f32 v7, v12, v8 op_sel:[0,0,1]
	s_mov_b32 s25, 0x24000
	v_add_co_u32_e32 v8, vcc, s25, v0
	s_mov_b64 s[34:35], 0x24000
	s_nop 0
	v_addc_co_u32_e32 v9, vcc, 0, v1, vcc
	v_lshl_add_u64 v[2:3], v[0:1], 0, s[34:35]
	s_mov_b32 s98, 0xffff0000
	s_mov_b32 s99, 0xffff0000
	v_mov_b32_e32 v178, 0x78
	v_mov_b32_e32 v179, 0
	v_permlane16_swap_b32_e32 v4, v6
	v_permlane16_swap_b32_e32 v5, v7
	v_cndmask_b32_e64 v178, 0, v178, s[98:99]
	v_cndmask_b32_e64 v176, v8, v2, s[98:99]
	v_cndmask_b32_e64 v177, v9, v3, s[98:99]
	v_lshl_add_u64 v[176:177], v[176:177], 0, v[178:179]
	global_store_dwordx4 v[176:177], v[4:7], off
	s_nop 1
	v_mul_f32_e32 v4, 0x3b800000, v68
	v_med3_f32 v5, v4, s72, v204
	v_mul_f32_e32 v4, 0x3b800000, v56
	v_med3_f32 v6, v4, s72, v204
	v_mul_f32_e32 v4, 0x3b800000, v69
	v_med3_f32 v7, v4, s72, v204
	v_mul_f32_e32 v4, 0x3b800000, v57
	v_med3_f32 v8, v4, s72, v204
	v_mul_f32_e32 v4, 0x3b800000, v70
	v_med3_f32 v9, v4, s72, v204
	v_mul_f32_e32 v4, 0x3b800000, v58
	v_med3_f32 v10, v4, s72, v204
	v_mul_f32_e32 v4, 0x3b800000, v71
	v_med3_f32 v11, v4, s72, v204
	v_mov_b32_e32 v4, 0
	v_cvt_pk_fp8_f32 v4, v5, v7
	v_mov_b32_e32 v5, 0
	v_cvt_pk_fp8_f32 v5, v6, v8
	v_mul_f32_e32 v6, 0x3b800000, v59
	v_med3_f32 v6, v6, s72, v204
	v_cvt_pk_fp8_f32 v4, v9, v11 op_sel:[0,0,1]
	v_cvt_pk_fp8_f32 v5, v10, v6 op_sel:[0,0,1]
	v_mul_f32_e32 v6, 0x3b800000, v64
	v_med3_f32 v7, v6, s72, v204
	v_mul_f32_e32 v6, 0x3b800000, v52
	v_med3_f32 v8, v6, s72, v204
	v_mul_f32_e32 v6, 0x3b800000, v65
	v_med3_f32 v9, v6, s72, v204
	v_mul_f32_e32 v6, 0x3b800000, v53
	v_med3_f32 v10, v6, s72, v204
	v_mul_f32_e32 v6, 0x3b800000, v66
	v_med3_f32 v11, v6, s72, v204
	v_mul_f32_e32 v6, 0x3b800000, v54
	v_med3_f32 v12, v6, s72, v204
	v_mul_f32_e32 v6, 0x3b800000, v67
	v_med3_f32 v13, v6, s72, v204
	v_mov_b32_e32 v6, 0
	v_cvt_pk_fp8_f32 v6, v7, v9
	v_mov_b32_e32 v7, 0
	v_cvt_pk_fp8_f32 v7, v8, v10
	v_mul_f32_e32 v8, 0x3b800000, v55
	v_med3_f32 v8, v8, s72, v204
	v_cvt_pk_fp8_f32 v6, v11, v13 op_sel:[0,0,1]
	v_cvt_pk_fp8_f32 v7, v12, v8 op_sel:[0,0,1]
	s_mov_b32 s25, 0x28000
	v_add_co_u32_e32 v8, vcc, s25, v0
	s_mov_b64 s[34:35], 0x28000
	s_nop 0
	v_addc_co_u32_e32 v9, vcc, 0, v1, vcc
	v_lshl_add_u64 v[2:3], v[0:1], 0, s[34:35]
	s_mov_b32 s98, 0xffff0000
	s_mov_b32 s99, 0xffff0000
	v_mov_b32_e32 v178, 0x78
	v_mov_b32_e32 v179, 0
	v_permlane16_swap_b32_e32 v4, v6
	v_permlane16_swap_b32_e32 v5, v7
	v_cndmask_b32_e64 v178, 0, v178, s[98:99]
	v_cndmask_b32_e64 v176, v8, v2, s[98:99]
	v_cndmask_b32_e64 v177, v9, v3, s[98:99]
	v_lshl_add_u64 v[176:177], v[176:177], 0, v[178:179]
	global_store_dwordx4 v[176:177], v[4:7], off
	s_nop 1
	v_mul_f32_e32 v4, 0x3b800000, v44
	v_med3_f32 v5, v4, s72, v204
	v_mul_f32_e32 v4, 0x3b800000, v36
	v_med3_f32 v6, v4, s72, v204
	v_mul_f32_e32 v4, 0x3b800000, v45
	v_med3_f32 v7, v4, s72, v204
	v_mul_f32_e32 v4, 0x3b800000, v37
	v_med3_f32 v8, v4, s72, v204
	v_mul_f32_e32 v4, 0x3b800000, v46
	v_med3_f32 v9, v4, s72, v204
	v_mul_f32_e32 v4, 0x3b800000, v38
	v_med3_f32 v10, v4, s72, v204
	v_mul_f32_e32 v4, 0x3b800000, v47
	v_med3_f32 v11, v4, s72, v204
	v_mov_b32_e32 v4, 0
	v_cvt_pk_fp8_f32 v4, v5, v7
	v_mov_b32_e32 v5, 0
	v_cvt_pk_fp8_f32 v5, v6, v8
	v_mul_f32_e32 v6, 0x3b800000, v39
	v_med3_f32 v6, v6, s72, v204
	v_cvt_pk_fp8_f32 v4, v9, v11 op_sel:[0,0,1]
	v_cvt_pk_fp8_f32 v5, v10, v6 op_sel:[0,0,1]
	v_mul_f32_e32 v6, 0x3b800000, v40
	v_med3_f32 v7, v6, s72, v204
	v_mul_f32_e32 v6, 0x3b800000, v32
	v_med3_f32 v8, v6, s72, v204
	v_mul_f32_e32 v6, 0x3b800000, v41
	v_med3_f32 v9, v6, s72, v204
	v_mul_f32_e32 v6, 0x3b800000, v33
	v_med3_f32 v10, v6, s72, v204
	v_mul_f32_e32 v6, 0x3b800000, v42
	v_med3_f32 v11, v6, s72, v204
	v_mul_f32_e32 v6, 0x3b800000, v34
	v_med3_f32 v12, v6, s72, v204
	v_mul_f32_e32 v6, 0x3b800000, v43
	v_med3_f32 v13, v6, s72, v204
	v_mov_b32_e32 v6, 0
	v_cvt_pk_fp8_f32 v6, v7, v9
	v_mov_b32_e32 v7, 0
	v_cvt_pk_fp8_f32 v7, v8, v10
	v_mul_f32_e32 v8, 0x3b800000, v35
	s_mov_b64 s[34:35], 0x2c000
	v_med3_f32 v8, v8, s72, v204
	s_mov_b32 s25, 0x2c000
	v_lshl_add_u64 v[2:3], v[0:1], 0, s[34:35]
	v_cvt_pk_fp8_f32 v6, v11, v13 op_sel:[0,0,1]
	v_cvt_pk_fp8_f32 v7, v12, v8 op_sel:[0,0,1]
	v_add_co_u32_e32 v0, vcc, s25, v0
	v_readlane_b32 s74, v254, 58
	s_nop 0
	v_addc_co_u32_e32 v1, vcc, 0, v1, vcc
	s_andn2_b64 vcc, exec, s[4:5]
	s_mov_b64 s[4:5], -1
	s_mov_b32 s98, 0xffff0000
	s_mov_b32 s99, 0xffff0000
	v_mov_b32_e32 v178, 0x78
	v_mov_b32_e32 v179, 0
	v_permlane16_swap_b32_e32 v4, v6
	v_permlane16_swap_b32_e32 v5, v7
	v_cndmask_b32_e64 v178, 0, v178, s[98:99]
	v_cndmask_b32_e64 v176, v0, v2, s[98:99]
	v_cndmask_b32_e64 v177, v1, v3, s[98:99]
	v_lshl_add_u64 v[176:177], v[176:177], 0, v[178:179]
	global_store_dwordx4 v[176:177], v[4:7], off
	s_nop 1
	s_cbranch_vccnz .LBB0_909
	s_andn2_b64 vcc, exec, s[6:7]
	s_cbranch_vccnz .LBB0_908
	s_barrier
	s_branch .LBB0_908

.LBB0_1793:
	v_mul_f32_e32 v6, 0x3b800000, v152
	v_med3_f32 v8, v6, s74, v204
	v_mul_f32_e32 v6, 0x3b800000, v157
	v_med3_f32 v7, v6, s74, v204
	v_mul_f32_e32 v6, 0x3b800000, v153
	v_lshl_add_u32 v4, s16, 8, v184
	v_med3_f32 v9, v6, s74, v204
	v_mul_f32_e32 v6, 0x3b800000, v158
	v_ashrrev_i32_e32 v5, 31, v4
	v_med3_f32 v10, v6, s74, v204
	v_mul_f32_e32 v6, 0x3b800000, v154
	v_lshlrev_b64 v[0:1], 10, v[4:5]
	v_mul_f32_e32 v5, 0x3b800000, v156
	v_med3_f32 v11, v6, s74, v204
	v_mul_f32_e32 v6, 0x3b800000, v159
	v_med3_f32 v5, v5, s74, v204
	v_med3_f32 v12, v6, s74, v204
	v_mov_b32_e32 v6, 0
	v_cvt_pk_fp8_f32 v6, v5, v7
	v_mov_b32_e32 v7, 0
	v_cvt_pk_fp8_f32 v7, v8, v9
	v_mul_f32_e32 v8, 0x3b800000, v144
	v_mul_f32_e32 v5, 0x3b800000, v155
	v_cvt_pk_fp8_f32 v6, v10, v12 op_sel:[0,0,1]
	v_med3_f32 v10, v8, s74, v204
	v_mul_f32_e32 v8, 0x3b800000, v149
	v_med3_f32 v5, v5, s74, v204
	v_med3_f32 v9, v8, s74, v204
	v_mul_f32_e32 v8, 0x3b800000, v145
	v_cvt_pk_fp8_f32 v7, v11, v5 op_sel:[0,0,1]
	v_med3_f32 v11, v8, s74, v204
	v_mul_f32_e32 v8, 0x3b800000, v150
	v_med3_f32 v12, v8, s74, v204
	v_mul_f32_e32 v8, 0x3b800000, v146
	v_mul_f32_e32 v5, 0x3b800000, v148
	v_med3_f32 v13, v8, s74, v204
	v_mul_f32_e32 v8, 0x3b800000, v151
	v_med3_f32 v5, v5, s74, v204
	v_med3_f32 v14, v8, s74, v204
	v_mov_b32_e32 v8, 0
	v_cvt_pk_fp8_f32 v8, v5, v9
	v_mov_b32_e32 v9, 0
	v_cvt_pk_fp8_f32 v9, v10, v11
	v_mul_f32_e32 v5, 0x3b800000, v147
	v_med3_f32 v5, v5, s74, v204
	v_readlane_b32 s30, v254, 50
	v_lshl_or_b32 v2, s75, 8, v201
	v_cvt_pk_fp8_f32 v8, v12, v14 op_sel:[0,0,1]
	v_cvt_pk_fp8_f32 v9, v13, v5 op_sel:[0,0,1]
	v_readlane_b32 s31, v254, 51
	v_ashrrev_i32_e32 v3, 31, v2
	v_mul_f32_e32 v5, 0x3b800000, v140
	v_lshl_add_u64 v[0:1], s[30:31], 0, v[0:1]
	v_lshl_add_u64 v[0:1], v[0:1], 0, v[2:3]
	s_mov_b32 s98, 0xffff0000
	s_mov_b32 s99, 0xffff0000
	v_mov_b32_e32 v178, 0x78
	v_mov_b32_e32 v179, 0
	v_permlane16_swap_b32_e32 v6, v8
	v_permlane16_swap_b32_e32 v7, v9
	v_cndmask_b32_e64 v178, 0, v178, s[98:99]
	v_cndmask_b32_e64 v176, v0, v0, s[98:99]
	v_cndmask_b32_e64 v177, v1, v1, s[98:99]
	v_lshl_add_u64 v[176:177], v[176:177], 0, v[178:179]
	global_store_dwordx4 v[176:177], v[6:9], off
	s_nop 1
	v_mul_f32_e32 v8, 0x3b800000, v136
	v_med3_f32 v10, v8, s74, v204
	v_mul_f32_e32 v8, 0x3b800000, v141
	v_med3_f32 v9, v8, s74, v204
	v_mul_f32_e32 v8, 0x3b800000, v137
	v_med3_f32 v11, v8, s74, v204
	v_mul_f32_e32 v8, 0x3b800000, v142
	v_med3_f32 v12, v8, s74, v204
	v_mul_f32_e32 v8, 0x3b800000, v138
	v_med3_f32 v13, v8, s74, v204
	v_mul_f32_e32 v8, 0x3b800000, v143
	v_med3_f32 v5, v5, s74, v204
	v_med3_f32 v14, v8, s74, v204
	v_mov_b32_e32 v8, 0
	v_cvt_pk_fp8_f32 v8, v5, v9
	v_mov_b32_e32 v9, 0
	v_cvt_pk_fp8_f32 v9, v10, v11
	v_mul_f32_e32 v10, 0x3b800000, v128
	v_mul_f32_e32 v5, 0x3b800000, v139
	v_cvt_pk_fp8_f32 v8, v12, v14 op_sel:[0,0,1]
	v_med3_f32 v12, v10, s74, v204
	v_mul_f32_e32 v10, 0x3b800000, v133
	v_med3_f32 v5, v5, s74, v204
	v_med3_f32 v11, v10, s74, v204
	v_mul_f32_e32 v10, 0x3b800000, v129
	v_cvt_pk_fp8_f32 v9, v13, v5 op_sel:[0,0,1]
	v_med3_f32 v13, v10, s74, v204
	v_mul_f32_e32 v10, 0x3b800000, v134
	v_med3_f32 v14, v10, s74, v204
	v_mul_f32_e32 v10, 0x3b800000, v130
	v_mul_f32_e32 v5, 0x3b800000, v132
	v_med3_f32 v15, v10, s74, v204
	v_mul_f32_e32 v10, 0x3b800000, v135
	v_med3_f32 v5, v5, s74, v204
	v_med3_f32 v16, v10, s74, v204
	v_mov_b32_e32 v10, 0
	v_cvt_pk_fp8_f32 v10, v5, v11
	v_mov_b32_e32 v11, 0
	v_cvt_pk_fp8_f32 v11, v12, v13
	v_or_b32_e32 v6, 16, v4
	v_mul_f32_e32 v5, 0x3b800000, v131
	v_ashrrev_i32_e32 v7, 31, v6
	v_med3_f32 v5, v5, s74, v204
	v_lshlrev_b64 v[6:7], 10, v[6:7]
	v_cvt_pk_fp8_f32 v10, v14, v16 op_sel:[0,0,1]
	v_cvt_pk_fp8_f32 v11, v15, v5 op_sel:[0,0,1]
	v_lshl_add_u64 v[6:7], s[30:31], 0, v[6:7]
	v_lshl_add_u64 v[6:7], v[6:7], 0, v[2:3]
	s_mov_b32 s98, 0xffff0000
	s_mov_b32 s99, 0xffff0000
	v_mov_b32_e32 v178, 0x78
	v_mov_b32_e32 v179, 0
	v_permlane16_swap_b32_e32 v8, v10
	v_permlane16_swap_b32_e32 v9, v11
	v_cndmask_b32_e64 v178, 0, v178, s[98:99]
	v_cndmask_b32_e64 v176, v6, v6, s[98:99]
	v_cndmask_b32_e64 v177, v7, v7, s[98:99]
	v_lshl_add_u64 v[176:177], v[176:177], 0, v[178:179]
	global_store_dwordx4 v[176:177], v[8:11], off
	s_nop 1
	v_mul_f32_e32 v8, 0x3b800000, v120
	v_med3_f32 v10, v8, s74, v204
	v_mul_f32_e32 v8, 0x3b800000, v125
	v_med3_f32 v9, v8, s74, v204
	v_mul_f32_e32 v8, 0x3b800000, v121
	v_med3_f32 v11, v8, s74, v204
	v_mul_f32_e32 v8, 0x3b800000, v126
	v_med3_f32 v12, v8, s74, v204
	v_mul_f32_e32 v8, 0x3b800000, v122
	v_mul_f32_e32 v5, 0x3b800000, v124
	v_med3_f32 v13, v8, s74, v204
	v_mul_f32_e32 v8, 0x3b800000, v127
	v_med3_f32 v5, v5, s74, v204
	v_med3_f32 v14, v8, s74, v204
	v_mov_b32_e32 v8, 0
	v_cvt_pk_fp8_f32 v8, v5, v9
	v_mov_b32_e32 v9, 0
	v_cvt_pk_fp8_f32 v9, v10, v11
	v_mul_f32_e32 v10, 0x3b800000, v112
	v_mul_f32_e32 v5, 0x3b800000, v123
	v_cvt_pk_fp8_f32 v8, v12, v14 op_sel:[0,0,1]
	v_med3_f32 v12, v10, s74, v204
	v_mul_f32_e32 v10, 0x3b800000, v117
	v_med3_f32 v5, v5, s74, v204
	v_med3_f32 v11, v10, s74, v204
	v_mul_f32_e32 v10, 0x3b800000, v113
	v_cvt_pk_fp8_f32 v9, v13, v5 op_sel:[0,0,1]
	v_med3_f32 v13, v10, s74, v204
	v_mul_f32_e32 v10, 0x3b800000, v118
	v_med3_f32 v14, v10, s74, v204
	v_mul_f32_e32 v10, 0x3b800000, v114
	v_mul_f32_e32 v5, 0x3b800000, v116
	v_med3_f32 v15, v10, s74, v204
	v_mul_f32_e32 v10, 0x3b800000, v119
	v_med3_f32 v5, v5, s74, v204
	v_med3_f32 v16, v10, s74, v204
	v_mov_b32_e32 v10, 0
	v_cvt_pk_fp8_f32 v10, v5, v11
	v_mov_b32_e32 v11, 0
	v_cvt_pk_fp8_f32 v11, v12, v13
	v_or_b32_e32 v6, 32, v4
	v_mul_f32_e32 v5, 0x3b800000, v115
	v_ashrrev_i32_e32 v7, 31, v6
	v_med3_f32 v5, v5, s74, v204
	v_lshlrev_b64 v[6:7], 10, v[6:7]
	v_cvt_pk_fp8_f32 v10, v14, v16 op_sel:[0,0,1]
	v_cvt_pk_fp8_f32 v11, v15, v5 op_sel:[0,0,1]
	v_lshl_add_u64 v[6:7], s[30:31], 0, v[6:7]
	v_lshl_add_u64 v[6:7], v[6:7], 0, v[2:3]
	s_mov_b32 s98, 0xffff0000
	s_mov_b32 s99, 0xffff0000
	v_mov_b32_e32 v178, 0x78
	v_mov_b32_e32 v179, 0
	v_permlane16_swap_b32_e32 v8, v10
	v_permlane16_swap_b32_e32 v9, v11
	v_cndmask_b32_e64 v178, 0, v178, s[98:99]
	v_cndmask_b32_e64 v176, v6, v6, s[98:99]
	v_cndmask_b32_e64 v177, v7, v7, s[98:99]
	v_lshl_add_u64 v[176:177], v[176:177], 0, v[178:179]
	global_store_dwordx4 v[176:177], v[8:11], off
	s_nop 1
	v_mul_f32_e32 v6, 0x3b800000, v108
	v_med3_f32 v7, v6, s74, v204
	v_mul_f32_e32 v6, 0x3b800000, v104
	v_med3_f32 v8, v6, s74, v204
	v_mul_f32_e32 v6, 0x3b800000, v109
	v_med3_f32 v9, v6, s74, v204
	v_mul_f32_e32 v6, 0x3b800000, v105
	v_med3_f32 v10, v6, s74, v204
	v_mul_f32_e32 v6, 0x3b800000, v110
	v_med3_f32 v11, v6, s74, v204
	v_mul_f32_e32 v6, 0x3b800000, v106
	v_med3_f32 v12, v6, s74, v204
	v_mul_f32_e32 v6, 0x3b800000, v111
	v_med3_f32 v13, v6, s74, v204
	v_mov_b32_e32 v6, 0
	v_cvt_pk_fp8_f32 v6, v7, v9
	v_mov_b32_e32 v7, 0
	v_cvt_pk_fp8_f32 v7, v8, v10
	v_mul_f32_e32 v8, 0x3b800000, v107
	v_med3_f32 v8, v8, s74, v204
	v_cvt_pk_fp8_f32 v6, v11, v13 op_sel:[0,0,1]
	v_cvt_pk_fp8_f32 v7, v12, v8 op_sel:[0,0,1]
	v_mul_f32_e32 v8, 0x3b800000, v96
	v_med3_f32 v9, v8, s74, v204
	v_mul_f32_e32 v8, 0x3b800000, v88
	v_med3_f32 v10, v8, s74, v204
	v_mul_f32_e32 v8, 0x3b800000, v97
	v_med3_f32 v11, v8, s74, v204
	v_mul_f32_e32 v8, 0x3b800000, v89
	v_med3_f32 v12, v8, s74, v204
	v_mul_f32_e32 v8, 0x3b800000, v98
	v_med3_f32 v13, v8, s74, v204
	v_mul_f32_e32 v8, 0x3b800000, v90
	v_med3_f32 v14, v8, s74, v204
	v_mul_f32_e32 v8, 0x3b800000, v99
	v_med3_f32 v15, v8, s74, v204
	v_mov_b32_e32 v8, 0
	v_cvt_pk_fp8_f32 v8, v9, v11
	v_mov_b32_e32 v9, 0
	v_cvt_pk_fp8_f32 v9, v10, v12
	v_or_b32_e32 v4, 48, v4
	v_ashrrev_i32_e32 v5, 31, v4
	v_mul_f32_e32 v10, 0x3b800000, v91
	v_lshlrev_b64 v[4:5], 10, v[4:5]
	v_med3_f32 v10, v10, s74, v204
	v_cvt_pk_fp8_f32 v8, v13, v15 op_sel:[0,0,1]
	v_cvt_pk_fp8_f32 v9, v14, v10 op_sel:[0,0,1]
	v_lshl_add_u64 v[4:5], s[30:31], 0, v[4:5]
	v_lshl_add_u64 v[2:3], v[4:5], 0, v[2:3]
	v_mul_f32_e32 v4, 0x3b800000, v84
	v_med3_f32 v5, v4, s74, v204
	v_mul_f32_e32 v4, 0x3b800000, v76
	s_mov_b32 s98, 0xffff0000
	s_mov_b32 s99, 0xffff0000
	v_mov_b32_e32 v178, 0x78
	v_mov_b32_e32 v179, 0
	v_permlane16_swap_b32_e32 v6, v8
	v_permlane16_swap_b32_e32 v7, v9
	v_cndmask_b32_e64 v178, 0, v178, s[98:99]
	v_cndmask_b32_e64 v176, v2, v2, s[98:99]
	v_cndmask_b32_e64 v177, v3, v3, s[98:99]
	v_lshl_add_u64 v[176:177], v[176:177], 0, v[178:179]
	global_store_dwordx4 v[176:177], v[6:9], off
	s_nop 1
	v_med3_f32 v6, v4, s74, v204
	v_mul_f32_e32 v4, 0x3b800000, v85
	v_med3_f32 v7, v4, s74, v204
	v_mul_f32_e32 v4, 0x3b800000, v77
	v_med3_f32 v8, v4, s74, v204
	v_mul_f32_e32 v4, 0x3b800000, v86
	v_med3_f32 v9, v4, s74, v204
	v_mul_f32_e32 v4, 0x3b800000, v78
	v_med3_f32 v10, v4, s74, v204
	v_mul_f32_e32 v4, 0x3b800000, v87
	v_med3_f32 v11, v4, s74, v204
	v_mov_b32_e32 v4, 0
	v_cvt_pk_fp8_f32 v4, v5, v7
	v_mov_b32_e32 v5, 0
	v_cvt_pk_fp8_f32 v5, v6, v8
	v_mul_f32_e32 v6, 0x3b800000, v79
	v_med3_f32 v6, v6, s74, v204
	v_cvt_pk_fp8_f32 v4, v9, v11 op_sel:[0,0,1]
	v_cvt_pk_fp8_f32 v5, v10, v6 op_sel:[0,0,1]
	v_mul_f32_e32 v6, 0x3b800000, v100
	v_med3_f32 v7, v6, s74, v204
	v_mul_f32_e32 v6, 0x3b800000, v92
	v_med3_f32 v8, v6, s74, v204
	v_mul_f32_e32 v6, 0x3b800000, v101
	v_med3_f32 v9, v6, s74, v204
	v_mul_f32_e32 v6, 0x3b800000, v93
	v_med3_f32 v10, v6, s74, v204
	v_mul_f32_e32 v6, 0x3b800000, v102
	v_med3_f32 v11, v6, s74, v204
	v_mul_f32_e32 v6, 0x3b800000, v94
	v_med3_f32 v12, v6, s74, v204
	v_mul_f32_e32 v6, 0x3b800000, v103
	v_med3_f32 v13, v6, s74, v204
	v_mov_b32_e32 v6, 0
	v_cvt_pk_fp8_f32 v6, v7, v9
	v_mov_b32_e32 v7, 0
	v_cvt_pk_fp8_f32 v7, v8, v10
	v_mul_f32_e32 v8, 0x3b800000, v95
	v_med3_f32 v8, v8, s74, v204
	v_cvt_pk_fp8_f32 v6, v11, v13 op_sel:[0,0,1]
	v_cvt_pk_fp8_f32 v7, v12, v8 op_sel:[0,0,1]
	s_mov_b32 s15, 0x20000
	v_add_co_u32_e32 v8, vcc, s15, v0
	s_mov_b64 s[30:31], 0x20000
	s_nop 0
	v_addc_co_u32_e32 v9, vcc, 0, v1, vcc
	v_lshl_add_u64 v[2:3], v[0:1], 0, s[30:31]
	s_mov_b32 s98, 0xffff0000
	s_mov_b32 s99, 0xffff0000
	v_mov_b32_e32 v178, 0x78
	v_mov_b32_e32 v179, 0
	v_permlane16_swap_b32_e32 v4, v6
	v_permlane16_swap_b32_e32 v5, v7
	v_cndmask_b32_e64 v178, 0, v178, s[98:99]
	v_cndmask_b32_e64 v176, v8, v2, s[98:99]
	v_cndmask_b32_e64 v177, v9, v3, s[98:99]
	v_lshl_add_u64 v[176:177], v[176:177], 0, v[178:179]
	global_store_dwordx4 v[176:177], v[4:7], off
	s_nop 1
	v_mul_f32_e32 v4, 0x3b800000, v60
	v_med3_f32 v5, v4, s74, v204
	v_mul_f32_e32 v4, 0x3b800000, v48
	v_med3_f32 v6, v4, s74, v204
	v_mul_f32_e32 v4, 0x3b800000, v61
	v_med3_f32 v7, v4, s74, v204
	v_mul_f32_e32 v4, 0x3b800000, v49
	v_med3_f32 v8, v4, s74, v204
	v_mul_f32_e32 v4, 0x3b800000, v62
	v_med3_f32 v9, v4, s74, v204
	v_mul_f32_e32 v4, 0x3b800000, v50
	v_med3_f32 v10, v4, s74, v204
	v_mul_f32_e32 v4, 0x3b800000, v63
	v_med3_f32 v11, v4, s74, v204
	v_mov_b32_e32 v4, 0
	v_cvt_pk_fp8_f32 v4, v5, v7
	v_mov_b32_e32 v5, 0
	v_cvt_pk_fp8_f32 v5, v6, v8
	v_mul_f32_e32 v6, 0x3b800000, v51
	v_med3_f32 v6, v6, s74, v204
	v_cvt_pk_fp8_f32 v4, v9, v11 op_sel:[0,0,1]
	v_cvt_pk_fp8_f32 v5, v10, v6 op_sel:[0,0,1]
	v_mul_f32_e32 v6, 0x3b800000, v80
	v_med3_f32 v7, v6, s74, v204
	v_mul_f32_e32 v6, 0x3b800000, v72
	v_med3_f32 v8, v6, s74, v204
	v_mul_f32_e32 v6, 0x3b800000, v81
	v_med3_f32 v9, v6, s74, v204
	v_mul_f32_e32 v6, 0x3b800000, v73
	v_med3_f32 v10, v6, s74, v204
	v_mul_f32_e32 v6, 0x3b800000, v82
	v_med3_f32 v11, v6, s74, v204
	v_mul_f32_e32 v6, 0x3b800000, v74
	v_med3_f32 v12, v6, s74, v204
	v_mul_f32_e32 v6, 0x3b800000, v83
	v_med3_f32 v13, v6, s74, v204
	v_mov_b32_e32 v6, 0
	v_cvt_pk_fp8_f32 v6, v7, v9
	v_mov_b32_e32 v7, 0
	v_cvt_pk_fp8_f32 v7, v8, v10
	v_mul_f32_e32 v8, 0x3b800000, v75
	v_med3_f32 v8, v8, s74, v204
	v_cvt_pk_fp8_f32 v6, v11, v13 op_sel:[0,0,1]
	v_cvt_pk_fp8_f32 v7, v12, v8 op_sel:[0,0,1]
	s_mov_b32 s15, 0x24000
	v_add_co_u32_e32 v8, vcc, s15, v0
	s_mov_b64 s[30:31], 0x24000
	s_nop 0
	v_addc_co_u32_e32 v9, vcc, 0, v1, vcc
	v_lshl_add_u64 v[2:3], v[0:1], 0, s[30:31]
	s_mov_b32 s98, 0xffff0000
	s_mov_b32 s99, 0xffff0000
	v_mov_b32_e32 v178, 0x78
	v_mov_b32_e32 v179, 0
	v_permlane16_swap_b32_e32 v4, v6
	v_permlane16_swap_b32_e32 v5, v7
	v_cndmask_b32_e64 v178, 0, v178, s[98:99]
	v_cndmask_b32_e64 v176, v8, v2, s[98:99]
	v_cndmask_b32_e64 v177, v9, v3, s[98:99]
	v_lshl_add_u64 v[176:177], v[176:177], 0, v[178:179]
	global_store_dwordx4 v[176:177], v[4:7], off
	s_nop 1
	v_mul_f32_e32 v4, 0x3b800000, v68
	v_med3_f32 v5, v4, s74, v204
	v_mul_f32_e32 v4, 0x3b800000, v56
	v_med3_f32 v6, v4, s74, v204
	v_mul_f32_e32 v4, 0x3b800000, v69
	v_med3_f32 v7, v4, s74, v204
	v_mul_f32_e32 v4, 0x3b800000, v57
	v_med3_f32 v8, v4, s74, v204
	v_mul_f32_e32 v4, 0x3b800000, v70
	v_med3_f32 v9, v4, s74, v204
	v_mul_f32_e32 v4, 0x3b800000, v58
	v_med3_f32 v10, v4, s74, v204
	v_mul_f32_e32 v4, 0x3b800000, v71
	v_med3_f32 v11, v4, s74, v204
	v_mov_b32_e32 v4, 0
	v_cvt_pk_fp8_f32 v4, v5, v7
	v_mov_b32_e32 v5, 0
	v_cvt_pk_fp8_f32 v5, v6, v8
	v_mul_f32_e32 v6, 0x3b800000, v59
	v_med3_f32 v6, v6, s74, v204
	v_cvt_pk_fp8_f32 v4, v9, v11 op_sel:[0,0,1]
	v_cvt_pk_fp8_f32 v5, v10, v6 op_sel:[0,0,1]
	v_mul_f32_e32 v6, 0x3b800000, v64
	v_med3_f32 v7, v6, s74, v204
	v_mul_f32_e32 v6, 0x3b800000, v52
	v_med3_f32 v8, v6, s74, v204
	v_mul_f32_e32 v6, 0x3b800000, v65
	v_med3_f32 v9, v6, s74, v204
	v_mul_f32_e32 v6, 0x3b800000, v53
	v_med3_f32 v10, v6, s74, v204
	v_mul_f32_e32 v6, 0x3b800000, v66
	v_med3_f32 v11, v6, s74, v204
	v_mul_f32_e32 v6, 0x3b800000, v54
	v_med3_f32 v12, v6, s74, v204
	v_mul_f32_e32 v6, 0x3b800000, v67
	v_med3_f32 v13, v6, s74, v204
	v_mov_b32_e32 v6, 0
	v_cvt_pk_fp8_f32 v6, v7, v9
	v_mov_b32_e32 v7, 0
	v_cvt_pk_fp8_f32 v7, v8, v10
	v_mul_f32_e32 v8, 0x3b800000, v55
	v_med3_f32 v8, v8, s74, v204
	v_cvt_pk_fp8_f32 v6, v11, v13 op_sel:[0,0,1]
	v_cvt_pk_fp8_f32 v7, v12, v8 op_sel:[0,0,1]
	s_mov_b32 s15, 0x28000
	v_add_co_u32_e32 v8, vcc, s15, v0
	s_mov_b64 s[30:31], 0x28000
	s_nop 0
	v_addc_co_u32_e32 v9, vcc, 0, v1, vcc
	v_lshl_add_u64 v[2:3], v[0:1], 0, s[30:31]
	s_mov_b32 s98, 0xffff0000
	s_mov_b32 s99, 0xffff0000
	v_mov_b32_e32 v178, 0x78
	v_mov_b32_e32 v179, 0
	v_permlane16_swap_b32_e32 v4, v6
	v_permlane16_swap_b32_e32 v5, v7
	v_cndmask_b32_e64 v178, 0, v178, s[98:99]
	v_cndmask_b32_e64 v176, v8, v2, s[98:99]
	v_cndmask_b32_e64 v177, v9, v3, s[98:99]
	v_lshl_add_u64 v[176:177], v[176:177], 0, v[178:179]
	global_store_dwordx4 v[176:177], v[4:7], off
	s_nop 1
	v_mul_f32_e32 v4, 0x3b800000, v44
	v_med3_f32 v5, v4, s74, v204
	v_mul_f32_e32 v4, 0x3b800000, v36
	v_med3_f32 v6, v4, s74, v204
	v_mul_f32_e32 v4, 0x3b800000, v45
	v_med3_f32 v7, v4, s74, v204
	v_mul_f32_e32 v4, 0x3b800000, v37
	v_med3_f32 v8, v4, s74, v204
	v_mul_f32_e32 v4, 0x3b800000, v46
	v_med3_f32 v9, v4, s74, v204
	v_mul_f32_e32 v4, 0x3b800000, v38
	v_med3_f32 v10, v4, s74, v204
	v_mul_f32_e32 v4, 0x3b800000, v47
	v_med3_f32 v11, v4, s74, v204
	v_mov_b32_e32 v4, 0
	v_cvt_pk_fp8_f32 v4, v5, v7
	v_mov_b32_e32 v5, 0
	v_cvt_pk_fp8_f32 v5, v6, v8
	v_mul_f32_e32 v6, 0x3b800000, v39
	v_med3_f32 v6, v6, s74, v204
	v_cvt_pk_fp8_f32 v4, v9, v11 op_sel:[0,0,1]
	v_cvt_pk_fp8_f32 v5, v10, v6 op_sel:[0,0,1]
	v_mul_f32_e32 v6, 0x3b800000, v40
	v_med3_f32 v7, v6, s74, v204
	v_mul_f32_e32 v6, 0x3b800000, v32
	v_med3_f32 v8, v6, s74, v204
	v_mul_f32_e32 v6, 0x3b800000, v41
	v_med3_f32 v9, v6, s74, v204
	v_mul_f32_e32 v6, 0x3b800000, v33
	v_med3_f32 v10, v6, s74, v204
	v_mul_f32_e32 v6, 0x3b800000, v42
	v_med3_f32 v11, v6, s74, v204
	v_mul_f32_e32 v6, 0x3b800000, v34
	v_med3_f32 v12, v6, s74, v204
	v_mul_f32_e32 v6, 0x3b800000, v43
	v_med3_f32 v13, v6, s74, v204
	v_mov_b32_e32 v6, 0
	v_cvt_pk_fp8_f32 v6, v7, v9
	v_mov_b32_e32 v7, 0
	v_cvt_pk_fp8_f32 v7, v8, v10
	v_mul_f32_e32 v8, 0x3b800000, v35
	s_mov_b64 s[30:31], 0x2c000
	v_med3_f32 v8, v8, s74, v204
	s_mov_b32 s15, 0x2c000
	v_lshl_add_u64 v[2:3], v[0:1], 0, s[30:31]
	v_cvt_pk_fp8_f32 v6, v11, v13 op_sel:[0,0,1]
	v_cvt_pk_fp8_f32 v7, v12, v8 op_sel:[0,0,1]
	v_add_co_u32_e32 v0, vcc, s15, v0
	s_nop 1
	v_addc_co_u32_e32 v1, vcc, 0, v1, vcc
	s_andn2_b64 vcc, exec, s[4:5]
	s_mov_b64 s[4:5], -1
	s_mov_b32 s98, 0xffff0000
	s_mov_b32 s99, 0xffff0000
	v_mov_b32_e32 v178, 0x78
	v_mov_b32_e32 v179, 0
	v_permlane16_swap_b32_e32 v4, v6
	v_permlane16_swap_b32_e32 v5, v7
	v_cndmask_b32_e64 v178, 0, v178, s[98:99]
	v_cndmask_b32_e64 v176, v0, v2, s[98:99]
	v_cndmask_b32_e64 v177, v1, v3, s[98:99]
	v_lshl_add_u64 v[176:177], v[176:177], 0, v[178:179]
	global_store_dwordx4 v[176:177], v[4:7], off
	s_nop 1
	s_cbranch_vccnz .LBB0_1786
	s_andn2_b64 vcc, exec, s[6:7]
	s_cbranch_vccnz .LBB0_1785
	s_barrier
	s_branch .LBB0_1785

.LBB0_2672:
	v_mul_f32_e32 v6, 0x3b800000, v152
	v_med3_f32 v8, v6, s74, v204
	v_mul_f32_e32 v6, 0x3b800000, v157
	v_med3_f32 v7, v6, s74, v204
	v_mul_f32_e32 v6, 0x3b800000, v153
	v_lshl_add_u32 v4, s16, 8, v184
	v_med3_f32 v9, v6, s74, v204
	v_mul_f32_e32 v6, 0x3b800000, v158
	v_ashrrev_i32_e32 v5, 31, v4
	v_med3_f32 v10, v6, s74, v204
	v_mul_f32_e32 v6, 0x3b800000, v154
	v_lshlrev_b64 v[0:1], 10, v[4:5]
	v_mul_f32_e32 v5, 0x3b800000, v156
	v_med3_f32 v11, v6, s74, v204
	v_mul_f32_e32 v6, 0x3b800000, v159
	v_med3_f32 v5, v5, s74, v204
	v_med3_f32 v12, v6, s74, v204
	v_mov_b32_e32 v6, 0
	v_cvt_pk_fp8_f32 v6, v5, v7
	v_mov_b32_e32 v7, 0
	v_cvt_pk_fp8_f32 v7, v8, v9
	v_mul_f32_e32 v8, 0x3b800000, v144
	v_mul_f32_e32 v5, 0x3b800000, v155
	v_cvt_pk_fp8_f32 v6, v10, v12 op_sel:[0,0,1]
	v_med3_f32 v10, v8, s74, v204
	v_mul_f32_e32 v8, 0x3b800000, v149
	v_med3_f32 v5, v5, s74, v204
	v_med3_f32 v9, v8, s74, v204
	v_mul_f32_e32 v8, 0x3b800000, v145
	v_cvt_pk_fp8_f32 v7, v11, v5 op_sel:[0,0,1]
	v_med3_f32 v11, v8, s74, v204
	v_mul_f32_e32 v8, 0x3b800000, v150
	v_med3_f32 v12, v8, s74, v204
	v_mul_f32_e32 v8, 0x3b800000, v146
	v_mul_f32_e32 v5, 0x3b800000, v148
	v_med3_f32 v13, v8, s74, v204
	v_mul_f32_e32 v8, 0x3b800000, v151
	v_med3_f32 v5, v5, s74, v204
	v_med3_f32 v14, v8, s74, v204
	v_mov_b32_e32 v8, 0
	v_cvt_pk_fp8_f32 v8, v5, v9
	v_mov_b32_e32 v9, 0
	v_cvt_pk_fp8_f32 v9, v10, v11
	v_mul_f32_e32 v5, 0x3b800000, v147
	v_med3_f32 v5, v5, s74, v204
	v_readlane_b32 s24, v254, 50
	v_lshl_or_b32 v2, s75, 8, v201
	v_cvt_pk_fp8_f32 v8, v12, v14 op_sel:[0,0,1]
	v_cvt_pk_fp8_f32 v9, v13, v5 op_sel:[0,0,1]
	v_readlane_b32 s25, v254, 51
	v_ashrrev_i32_e32 v3, 31, v2
	v_mul_f32_e32 v5, 0x3b800000, v140
	v_lshl_add_u64 v[0:1], s[24:25], 0, v[0:1]
	v_lshl_add_u64 v[0:1], v[0:1], 0, v[2:3]
	s_mov_b32 s98, 0xffff0000
	s_mov_b32 s99, 0xffff0000
	v_mov_b32_e32 v178, 0x78
	v_mov_b32_e32 v179, 0
	v_permlane16_swap_b32_e32 v6, v8
	v_permlane16_swap_b32_e32 v7, v9
	v_cndmask_b32_e64 v178, 0, v178, s[98:99]
	v_cndmask_b32_e64 v176, v0, v0, s[98:99]
	v_cndmask_b32_e64 v177, v1, v1, s[98:99]
	v_lshl_add_u64 v[176:177], v[176:177], 0, v[178:179]
	global_store_dwordx4 v[176:177], v[6:9], off
	s_nop 1
	v_mul_f32_e32 v8, 0x3b800000, v136
	v_med3_f32 v10, v8, s74, v204
	v_mul_f32_e32 v8, 0x3b800000, v141
	v_med3_f32 v9, v8, s74, v204
	v_mul_f32_e32 v8, 0x3b800000, v137
	v_med3_f32 v11, v8, s74, v204
	v_mul_f32_e32 v8, 0x3b800000, v142
	v_med3_f32 v12, v8, s74, v204
	v_mul_f32_e32 v8, 0x3b800000, v138
	v_med3_f32 v13, v8, s74, v204
	v_mul_f32_e32 v8, 0x3b800000, v143
	v_med3_f32 v5, v5, s74, v204
	v_med3_f32 v14, v8, s74, v204
	v_mov_b32_e32 v8, 0
	v_cvt_pk_fp8_f32 v8, v5, v9
	v_mov_b32_e32 v9, 0
	v_cvt_pk_fp8_f32 v9, v10, v11
	v_mul_f32_e32 v10, 0x3b800000, v128
	v_mul_f32_e32 v5, 0x3b800000, v139
	v_cvt_pk_fp8_f32 v8, v12, v14 op_sel:[0,0,1]
	v_med3_f32 v12, v10, s74, v204
	v_mul_f32_e32 v10, 0x3b800000, v133
	v_med3_f32 v5, v5, s74, v204
	v_med3_f32 v11, v10, s74, v204
	v_mul_f32_e32 v10, 0x3b800000, v129
	v_cvt_pk_fp8_f32 v9, v13, v5 op_sel:[0,0,1]
	v_med3_f32 v13, v10, s74, v204
	v_mul_f32_e32 v10, 0x3b800000, v134
	v_med3_f32 v14, v10, s74, v204
	v_mul_f32_e32 v10, 0x3b800000, v130
	v_mul_f32_e32 v5, 0x3b800000, v132
	v_med3_f32 v15, v10, s74, v204
	v_mul_f32_e32 v10, 0x3b800000, v135
	v_med3_f32 v5, v5, s74, v204
	v_med3_f32 v16, v10, s74, v204
	v_mov_b32_e32 v10, 0
	v_cvt_pk_fp8_f32 v10, v5, v11
	v_mov_b32_e32 v11, 0
	v_cvt_pk_fp8_f32 v11, v12, v13
	v_or_b32_e32 v6, 16, v4
	v_mul_f32_e32 v5, 0x3b800000, v131
	v_ashrrev_i32_e32 v7, 31, v6
	v_med3_f32 v5, v5, s74, v204
	v_lshlrev_b64 v[6:7], 10, v[6:7]
	v_cvt_pk_fp8_f32 v10, v14, v16 op_sel:[0,0,1]
	v_cvt_pk_fp8_f32 v11, v15, v5 op_sel:[0,0,1]
	v_lshl_add_u64 v[6:7], s[24:25], 0, v[6:7]
	v_lshl_add_u64 v[6:7], v[6:7], 0, v[2:3]
	s_mov_b32 s98, 0xffff0000
	s_mov_b32 s99, 0xffff0000
	v_mov_b32_e32 v178, 0x78
	v_mov_b32_e32 v179, 0
	v_permlane16_swap_b32_e32 v8, v10
	v_permlane16_swap_b32_e32 v9, v11
	v_cndmask_b32_e64 v178, 0, v178, s[98:99]
	v_cndmask_b32_e64 v176, v6, v6, s[98:99]
	v_cndmask_b32_e64 v177, v7, v7, s[98:99]
	v_lshl_add_u64 v[176:177], v[176:177], 0, v[178:179]
	global_store_dwordx4 v[176:177], v[8:11], off
	s_nop 1
	v_mul_f32_e32 v8, 0x3b800000, v120
	v_med3_f32 v10, v8, s74, v204
	v_mul_f32_e32 v8, 0x3b800000, v125
	v_med3_f32 v9, v8, s74, v204
	v_mul_f32_e32 v8, 0x3b800000, v121
	v_med3_f32 v11, v8, s74, v204
	v_mul_f32_e32 v8, 0x3b800000, v126
	v_med3_f32 v12, v8, s74, v204
	v_mul_f32_e32 v8, 0x3b800000, v122
	v_mul_f32_e32 v5, 0x3b800000, v124
	v_med3_f32 v13, v8, s74, v204
	v_mul_f32_e32 v8, 0x3b800000, v127
	v_med3_f32 v5, v5, s74, v204
	v_med3_f32 v14, v8, s74, v204
	v_mov_b32_e32 v8, 0
	v_cvt_pk_fp8_f32 v8, v5, v9
	v_mov_b32_e32 v9, 0
	v_cvt_pk_fp8_f32 v9, v10, v11
	v_mul_f32_e32 v10, 0x3b800000, v112
	v_mul_f32_e32 v5, 0x3b800000, v123
	v_cvt_pk_fp8_f32 v8, v12, v14 op_sel:[0,0,1]
	v_med3_f32 v12, v10, s74, v204
	v_mul_f32_e32 v10, 0x3b800000, v117
	v_med3_f32 v5, v5, s74, v204
	v_med3_f32 v11, v10, s74, v204
	v_mul_f32_e32 v10, 0x3b800000, v113
	v_cvt_pk_fp8_f32 v9, v13, v5 op_sel:[0,0,1]
	v_med3_f32 v13, v10, s74, v204
	v_mul_f32_e32 v10, 0x3b800000, v118
	v_med3_f32 v14, v10, s74, v204
	v_mul_f32_e32 v10, 0x3b800000, v114
	v_mul_f32_e32 v5, 0x3b800000, v116
	v_med3_f32 v15, v10, s74, v204
	v_mul_f32_e32 v10, 0x3b800000, v119
	v_med3_f32 v5, v5, s74, v204
	v_med3_f32 v16, v10, s74, v204
	v_mov_b32_e32 v10, 0
	v_cvt_pk_fp8_f32 v10, v5, v11
	v_mov_b32_e32 v11, 0
	v_cvt_pk_fp8_f32 v11, v12, v13
	v_or_b32_e32 v6, 32, v4
	v_mul_f32_e32 v5, 0x3b800000, v115
	v_ashrrev_i32_e32 v7, 31, v6
	v_med3_f32 v5, v5, s74, v204
	v_lshlrev_b64 v[6:7], 10, v[6:7]
	v_cvt_pk_fp8_f32 v10, v14, v16 op_sel:[0,0,1]
	v_cvt_pk_fp8_f32 v11, v15, v5 op_sel:[0,0,1]
	v_lshl_add_u64 v[6:7], s[24:25], 0, v[6:7]
	v_lshl_add_u64 v[6:7], v[6:7], 0, v[2:3]
	s_mov_b32 s98, 0xffff0000
	s_mov_b32 s99, 0xffff0000
	v_mov_b32_e32 v178, 0x78
	v_mov_b32_e32 v179, 0
	v_permlane16_swap_b32_e32 v8, v10
	v_permlane16_swap_b32_e32 v9, v11
	v_cndmask_b32_e64 v178, 0, v178, s[98:99]
	v_cndmask_b32_e64 v176, v6, v6, s[98:99]
	v_cndmask_b32_e64 v177, v7, v7, s[98:99]
	v_lshl_add_u64 v[176:177], v[176:177], 0, v[178:179]
	global_store_dwordx4 v[176:177], v[8:11], off
	s_nop 1
	v_mul_f32_e32 v6, 0x3b800000, v108
	v_med3_f32 v7, v6, s74, v204
	v_mul_f32_e32 v6, 0x3b800000, v104
	v_med3_f32 v8, v6, s74, v204
	v_mul_f32_e32 v6, 0x3b800000, v109
	v_med3_f32 v9, v6, s74, v204
	v_mul_f32_e32 v6, 0x3b800000, v105
	v_med3_f32 v10, v6, s74, v204
	v_mul_f32_e32 v6, 0x3b800000, v110
	v_med3_f32 v11, v6, s74, v204
	v_mul_f32_e32 v6, 0x3b800000, v106
	v_med3_f32 v12, v6, s74, v204
	v_mul_f32_e32 v6, 0x3b800000, v111
	v_med3_f32 v13, v6, s74, v204
	v_mov_b32_e32 v6, 0
	v_cvt_pk_fp8_f32 v6, v7, v9
	v_mov_b32_e32 v7, 0
	v_cvt_pk_fp8_f32 v7, v8, v10
	v_mul_f32_e32 v8, 0x3b800000, v107
	v_med3_f32 v8, v8, s74, v204
	v_cvt_pk_fp8_f32 v6, v11, v13 op_sel:[0,0,1]
	v_cvt_pk_fp8_f32 v7, v12, v8 op_sel:[0,0,1]
	v_mul_f32_e32 v8, 0x3b800000, v96
	v_med3_f32 v9, v8, s74, v204
	v_mul_f32_e32 v8, 0x3b800000, v88
	v_med3_f32 v10, v8, s74, v204
	v_mul_f32_e32 v8, 0x3b800000, v97
	v_med3_f32 v11, v8, s74, v204
	v_mul_f32_e32 v8, 0x3b800000, v89
	v_med3_f32 v12, v8, s74, v204
	v_mul_f32_e32 v8, 0x3b800000, v98
	v_med3_f32 v13, v8, s74, v204
	v_mul_f32_e32 v8, 0x3b800000, v90
	v_med3_f32 v14, v8, s74, v204
	v_mul_f32_e32 v8, 0x3b800000, v99
	v_med3_f32 v15, v8, s74, v204
	v_mov_b32_e32 v8, 0
	v_cvt_pk_fp8_f32 v8, v9, v11
	v_mov_b32_e32 v9, 0
	v_cvt_pk_fp8_f32 v9, v10, v12
	v_or_b32_e32 v4, 48, v4
	v_ashrrev_i32_e32 v5, 31, v4
	v_mul_f32_e32 v10, 0x3b800000, v91
	v_lshlrev_b64 v[4:5], 10, v[4:5]
	v_med3_f32 v10, v10, s74, v204
	v_cvt_pk_fp8_f32 v8, v13, v15 op_sel:[0,0,1]
	v_cvt_pk_fp8_f32 v9, v14, v10 op_sel:[0,0,1]
	v_lshl_add_u64 v[4:5], s[24:25], 0, v[4:5]
	v_lshl_add_u64 v[2:3], v[4:5], 0, v[2:3]
	v_mul_f32_e32 v4, 0x3b800000, v84
	v_med3_f32 v5, v4, s74, v204
	v_mul_f32_e32 v4, 0x3b800000, v76
	s_mov_b32 s98, 0xffff0000
	s_mov_b32 s99, 0xffff0000
	v_mov_b32_e32 v178, 0x78
	v_mov_b32_e32 v179, 0
	v_permlane16_swap_b32_e32 v6, v8
	v_permlane16_swap_b32_e32 v7, v9
	v_cndmask_b32_e64 v178, 0, v178, s[98:99]
	v_cndmask_b32_e64 v176, v2, v2, s[98:99]
	v_cndmask_b32_e64 v177, v3, v3, s[98:99]
	v_lshl_add_u64 v[176:177], v[176:177], 0, v[178:179]
	global_store_dwordx4 v[176:177], v[6:9], off
	s_nop 1
	v_med3_f32 v6, v4, s74, v204
	v_mul_f32_e32 v4, 0x3b800000, v85
	v_med3_f32 v7, v4, s74, v204
	v_mul_f32_e32 v4, 0x3b800000, v77
	v_med3_f32 v8, v4, s74, v204
	v_mul_f32_e32 v4, 0x3b800000, v86
	v_med3_f32 v9, v4, s74, v204
	v_mul_f32_e32 v4, 0x3b800000, v78
	v_med3_f32 v10, v4, s74, v204
	v_mul_f32_e32 v4, 0x3b800000, v87
	v_med3_f32 v11, v4, s74, v204
	v_mov_b32_e32 v4, 0
	v_cvt_pk_fp8_f32 v4, v5, v7
	v_mov_b32_e32 v5, 0
	v_cvt_pk_fp8_f32 v5, v6, v8
	v_mul_f32_e32 v6, 0x3b800000, v79
	v_med3_f32 v6, v6, s74, v204
	v_cvt_pk_fp8_f32 v4, v9, v11 op_sel:[0,0,1]
	v_cvt_pk_fp8_f32 v5, v10, v6 op_sel:[0,0,1]
	v_mul_f32_e32 v6, 0x3b800000, v100
	v_med3_f32 v7, v6, s74, v204
	v_mul_f32_e32 v6, 0x3b800000, v92
	v_med3_f32 v8, v6, s74, v204
	v_mul_f32_e32 v6, 0x3b800000, v101
	v_med3_f32 v9, v6, s74, v204
	v_mul_f32_e32 v6, 0x3b800000, v93
	v_med3_f32 v10, v6, s74, v204
	v_mul_f32_e32 v6, 0x3b800000, v102
	v_med3_f32 v11, v6, s74, v204
	v_mul_f32_e32 v6, 0x3b800000, v94
	v_med3_f32 v12, v6, s74, v204
	v_mul_f32_e32 v6, 0x3b800000, v103
	v_med3_f32 v13, v6, s74, v204
	v_mov_b32_e32 v6, 0
	v_cvt_pk_fp8_f32 v6, v7, v9
	v_mov_b32_e32 v7, 0
	v_cvt_pk_fp8_f32 v7, v8, v10
	v_mul_f32_e32 v8, 0x3b800000, v95
	v_med3_f32 v8, v8, s74, v204
	v_cvt_pk_fp8_f32 v6, v11, v13 op_sel:[0,0,1]
	v_cvt_pk_fp8_f32 v7, v12, v8 op_sel:[0,0,1]
	s_mov_b32 s15, 0x20000
	v_add_co_u32_e32 v8, vcc, s15, v0
	s_mov_b64 s[24:25], 0x20000
	s_nop 0
	v_addc_co_u32_e32 v9, vcc, 0, v1, vcc
	v_lshl_add_u64 v[2:3], v[0:1], 0, s[24:25]
	s_mov_b32 s98, 0xffff0000
	s_mov_b32 s99, 0xffff0000
	v_mov_b32_e32 v178, 0x78
	v_mov_b32_e32 v179, 0
	v_permlane16_swap_b32_e32 v4, v6
	v_permlane16_swap_b32_e32 v5, v7
	v_cndmask_b32_e64 v178, 0, v178, s[98:99]
	v_cndmask_b32_e64 v176, v8, v2, s[98:99]
	v_cndmask_b32_e64 v177, v9, v3, s[98:99]
	v_lshl_add_u64 v[176:177], v[176:177], 0, v[178:179]
	global_store_dwordx4 v[176:177], v[4:7], off
	s_nop 1
	v_mul_f32_e32 v4, 0x3b800000, v60
	v_med3_f32 v5, v4, s74, v204
	v_mul_f32_e32 v4, 0x3b800000, v48
	v_med3_f32 v6, v4, s74, v204
	v_mul_f32_e32 v4, 0x3b800000, v61
	v_med3_f32 v7, v4, s74, v204
	v_mul_f32_e32 v4, 0x3b800000, v49
	v_med3_f32 v8, v4, s74, v204
	v_mul_f32_e32 v4, 0x3b800000, v62
	v_med3_f32 v9, v4, s74, v204
	v_mul_f32_e32 v4, 0x3b800000, v50
	v_med3_f32 v10, v4, s74, v204
	v_mul_f32_e32 v4, 0x3b800000, v63
	v_med3_f32 v11, v4, s74, v204
	v_mov_b32_e32 v4, 0
	v_cvt_pk_fp8_f32 v4, v5, v7
	v_mov_b32_e32 v5, 0
	v_cvt_pk_fp8_f32 v5, v6, v8
	v_mul_f32_e32 v6, 0x3b800000, v51
	v_med3_f32 v6, v6, s74, v204
	v_cvt_pk_fp8_f32 v4, v9, v11 op_sel:[0,0,1]
	v_cvt_pk_fp8_f32 v5, v10, v6 op_sel:[0,0,1]
	v_mul_f32_e32 v6, 0x3b800000, v80
	v_med3_f32 v7, v6, s74, v204
	v_mul_f32_e32 v6, 0x3b800000, v72
	v_med3_f32 v8, v6, s74, v204
	v_mul_f32_e32 v6, 0x3b800000, v81
	v_med3_f32 v9, v6, s74, v204
	v_mul_f32_e32 v6, 0x3b800000, v73
	v_med3_f32 v10, v6, s74, v204
	v_mul_f32_e32 v6, 0x3b800000, v82
	v_med3_f32 v11, v6, s74, v204
	v_mul_f32_e32 v6, 0x3b800000, v74
	v_med3_f32 v12, v6, s74, v204
	v_mul_f32_e32 v6, 0x3b800000, v83
	v_med3_f32 v13, v6, s74, v204
	v_mov_b32_e32 v6, 0
	v_cvt_pk_fp8_f32 v6, v7, v9
	v_mov_b32_e32 v7, 0
	v_cvt_pk_fp8_f32 v7, v8, v10
	v_mul_f32_e32 v8, 0x3b800000, v75
	v_med3_f32 v8, v8, s74, v204
	v_cvt_pk_fp8_f32 v6, v11, v13 op_sel:[0,0,1]
	v_cvt_pk_fp8_f32 v7, v12, v8 op_sel:[0,0,1]
	s_mov_b32 s15, 0x24000
	v_add_co_u32_e32 v8, vcc, s15, v0
	s_mov_b64 s[24:25], 0x24000
	s_nop 0
	v_addc_co_u32_e32 v9, vcc, 0, v1, vcc
	v_lshl_add_u64 v[2:3], v[0:1], 0, s[24:25]
	s_mov_b32 s98, 0xffff0000
	s_mov_b32 s99, 0xffff0000
	v_mov_b32_e32 v178, 0x78
	v_mov_b32_e32 v179, 0
	v_permlane16_swap_b32_e32 v4, v6
	v_permlane16_swap_b32_e32 v5, v7
	v_cndmask_b32_e64 v178, 0, v178, s[98:99]
	v_cndmask_b32_e64 v176, v8, v2, s[98:99]
	v_cndmask_b32_e64 v177, v9, v3, s[98:99]
	v_lshl_add_u64 v[176:177], v[176:177], 0, v[178:179]
	global_store_dwordx4 v[176:177], v[4:7], off
	s_nop 1
	v_mul_f32_e32 v4, 0x3b800000, v68
	v_med3_f32 v5, v4, s74, v204
	v_mul_f32_e32 v4, 0x3b800000, v56
	v_med3_f32 v6, v4, s74, v204
	v_mul_f32_e32 v4, 0x3b800000, v69
	v_med3_f32 v7, v4, s74, v204
	v_mul_f32_e32 v4, 0x3b800000, v57
	v_med3_f32 v8, v4, s74, v204
	v_mul_f32_e32 v4, 0x3b800000, v70
	v_med3_f32 v9, v4, s74, v204
	v_mul_f32_e32 v4, 0x3b800000, v58
	v_med3_f32 v10, v4, s74, v204
	v_mul_f32_e32 v4, 0x3b800000, v71
	v_med3_f32 v11, v4, s74, v204
	v_mov_b32_e32 v4, 0
	v_cvt_pk_fp8_f32 v4, v5, v7
	v_mov_b32_e32 v5, 0
	v_cvt_pk_fp8_f32 v5, v6, v8
	v_mul_f32_e32 v6, 0x3b800000, v59
	v_med3_f32 v6, v6, s74, v204
	v_cvt_pk_fp8_f32 v4, v9, v11 op_sel:[0,0,1]
	v_cvt_pk_fp8_f32 v5, v10, v6 op_sel:[0,0,1]
	v_mul_f32_e32 v6, 0x3b800000, v64
	v_med3_f32 v7, v6, s74, v204
	v_mul_f32_e32 v6, 0x3b800000, v52
	v_med3_f32 v8, v6, s74, v204
	v_mul_f32_e32 v6, 0x3b800000, v65
	v_med3_f32 v9, v6, s74, v204
	v_mul_f32_e32 v6, 0x3b800000, v53
	v_med3_f32 v10, v6, s74, v204
	v_mul_f32_e32 v6, 0x3b800000, v66
	v_med3_f32 v11, v6, s74, v204
	v_mul_f32_e32 v6, 0x3b800000, v54
	v_med3_f32 v12, v6, s74, v204
	v_mul_f32_e32 v6, 0x3b800000, v67
	v_med3_f32 v13, v6, s74, v204
	v_mov_b32_e32 v6, 0
	v_cvt_pk_fp8_f32 v6, v7, v9
	v_mov_b32_e32 v7, 0
	v_cvt_pk_fp8_f32 v7, v8, v10
	v_mul_f32_e32 v8, 0x3b800000, v55
	v_med3_f32 v8, v8, s74, v204
	v_cvt_pk_fp8_f32 v6, v11, v13 op_sel:[0,0,1]
	v_cvt_pk_fp8_f32 v7, v12, v8 op_sel:[0,0,1]
	s_mov_b32 s15, 0x28000
	v_add_co_u32_e32 v8, vcc, s15, v0
	s_mov_b64 s[24:25], 0x28000
	s_nop 0
	v_addc_co_u32_e32 v9, vcc, 0, v1, vcc
	v_lshl_add_u64 v[2:3], v[0:1], 0, s[24:25]
	s_mov_b32 s98, 0xffff0000
	s_mov_b32 s99, 0xffff0000
	v_mov_b32_e32 v178, 0x78
	v_mov_b32_e32 v179, 0
	v_permlane16_swap_b32_e32 v4, v6
	v_permlane16_swap_b32_e32 v5, v7
	v_cndmask_b32_e64 v178, 0, v178, s[98:99]
	v_cndmask_b32_e64 v176, v8, v2, s[98:99]
	v_cndmask_b32_e64 v177, v9, v3, s[98:99]
	v_lshl_add_u64 v[176:177], v[176:177], 0, v[178:179]
	global_store_dwordx4 v[176:177], v[4:7], off
	s_nop 1
	v_mul_f32_e32 v4, 0x3b800000, v44
	v_med3_f32 v5, v4, s74, v204
	v_mul_f32_e32 v4, 0x3b800000, v36
	v_med3_f32 v6, v4, s74, v204
	v_mul_f32_e32 v4, 0x3b800000, v45
	v_med3_f32 v7, v4, s74, v204
	v_mul_f32_e32 v4, 0x3b800000, v37
	v_med3_f32 v8, v4, s74, v204
	v_mul_f32_e32 v4, 0x3b800000, v46
	v_med3_f32 v9, v4, s74, v204
	v_mul_f32_e32 v4, 0x3b800000, v38
	v_med3_f32 v10, v4, s74, v204
	v_mul_f32_e32 v4, 0x3b800000, v47
	v_med3_f32 v11, v4, s74, v204
	v_mov_b32_e32 v4, 0
	v_cvt_pk_fp8_f32 v4, v5, v7
	v_mov_b32_e32 v5, 0
	v_cvt_pk_fp8_f32 v5, v6, v8
	v_mul_f32_e32 v6, 0x3b800000, v39
	v_med3_f32 v6, v6, s74, v204
	v_cvt_pk_fp8_f32 v4, v9, v11 op_sel:[0,0,1]
	v_cvt_pk_fp8_f32 v5, v10, v6 op_sel:[0,0,1]
	v_mul_f32_e32 v6, 0x3b800000, v40
	v_med3_f32 v7, v6, s74, v204
	v_mul_f32_e32 v6, 0x3b800000, v32
	v_med3_f32 v8, v6, s74, v204
	v_mul_f32_e32 v6, 0x3b800000, v41
	v_med3_f32 v9, v6, s74, v204
	v_mul_f32_e32 v6, 0x3b800000, v33
	v_med3_f32 v10, v6, s74, v204
	v_mul_f32_e32 v6, 0x3b800000, v42
	v_med3_f32 v11, v6, s74, v204
	v_mul_f32_e32 v6, 0x3b800000, v34
	v_med3_f32 v12, v6, s74, v204
	v_mul_f32_e32 v6, 0x3b800000, v43
	v_med3_f32 v13, v6, s74, v204
	v_mov_b32_e32 v6, 0
	v_cvt_pk_fp8_f32 v6, v7, v9
	v_mov_b32_e32 v7, 0
	v_cvt_pk_fp8_f32 v7, v8, v10
	v_mul_f32_e32 v8, 0x3b800000, v35
	s_mov_b64 s[24:25], 0x2c000
	v_med3_f32 v8, v8, s74, v204
	s_mov_b32 s15, 0x2c000
	v_lshl_add_u64 v[2:3], v[0:1], 0, s[24:25]
	v_cvt_pk_fp8_f32 v6, v11, v13 op_sel:[0,0,1]
	v_cvt_pk_fp8_f32 v7, v12, v8 op_sel:[0,0,1]
	v_add_co_u32_e32 v0, vcc, s15, v0
	s_nop 1
	v_addc_co_u32_e32 v1, vcc, 0, v1, vcc
	s_andn2_b64 vcc, exec, s[4:5]
	s_mov_b64 s[4:5], -1
	s_mov_b32 s98, 0xffff0000
	s_mov_b32 s99, 0xffff0000
	v_mov_b32_e32 v178, 0x78
	v_mov_b32_e32 v179, 0
	v_permlane16_swap_b32_e32 v4, v6
	v_permlane16_swap_b32_e32 v5, v7
	v_cndmask_b32_e64 v178, 0, v178, s[98:99]
	v_cndmask_b32_e64 v176, v0, v2, s[98:99]
	v_cndmask_b32_e64 v177, v1, v3, s[98:99]
	v_lshl_add_u64 v[176:177], v[176:177], 0, v[178:179]
	global_store_dwordx4 v[176:177], v[4:7], off
	s_nop 1
	s_cbranch_vccnz .LBB0_2665
	s_andn2_b64 vcc, exec, s[6:7]
	s_cbranch_vccnz .LBB0_2664
	s_barrier
	s_branch .LBB0_2664

.LBB0_3420:
	v_mul_f32_e32 v6, 0x3b800000, v152
	v_med3_f32 v8, v6, s72, v204
	v_mul_f32_e32 v6, 0x3b800000, v157
	v_med3_f32 v7, v6, s72, v204
	v_mul_f32_e32 v6, 0x3b800000, v153
	v_lshl_add_u32 v4, s16, 8, v184
	v_med3_f32 v9, v6, s72, v204
	v_mul_f32_e32 v6, 0x3b800000, v158
	v_ashrrev_i32_e32 v5, 31, v4
	v_med3_f32 v10, v6, s72, v204
	v_mul_f32_e32 v6, 0x3b800000, v154
	v_lshlrev_b64 v[0:1], 10, v[4:5]
	v_mul_f32_e32 v5, 0x3b800000, v156
	v_med3_f32 v11, v6, s72, v204
	v_mul_f32_e32 v6, 0x3b800000, v159
	v_med3_f32 v5, v5, s72, v204
	v_med3_f32 v12, v6, s72, v204
	v_mov_b32_e32 v6, 0
	v_cvt_pk_fp8_f32 v6, v5, v7
	v_mov_b32_e32 v7, 0
	v_cvt_pk_fp8_f32 v7, v8, v9
	v_mul_f32_e32 v8, 0x3b800000, v144
	v_mul_f32_e32 v5, 0x3b800000, v155
	v_cvt_pk_fp8_f32 v6, v10, v12 op_sel:[0,0,1]
	v_med3_f32 v10, v8, s72, v204
	v_mul_f32_e32 v8, 0x3b800000, v149
	v_med3_f32 v5, v5, s72, v204
	v_med3_f32 v9, v8, s72, v204
	v_mul_f32_e32 v8, 0x3b800000, v145
	v_cvt_pk_fp8_f32 v7, v11, v5 op_sel:[0,0,1]
	v_med3_f32 v11, v8, s72, v204
	v_mul_f32_e32 v8, 0x3b800000, v150
	v_med3_f32 v12, v8, s72, v204
	v_mul_f32_e32 v8, 0x3b800000, v146
	v_mul_f32_e32 v5, 0x3b800000, v148
	v_med3_f32 v13, v8, s72, v204
	v_mul_f32_e32 v8, 0x3b800000, v151
	v_med3_f32 v5, v5, s72, v204
	v_med3_f32 v14, v8, s72, v204
	v_mov_b32_e32 v8, 0
	v_cvt_pk_fp8_f32 v8, v5, v9
	v_mov_b32_e32 v9, 0
	v_cvt_pk_fp8_f32 v9, v10, v11
	v_mul_f32_e32 v5, 0x3b800000, v147
	v_med3_f32 v5, v5, s72, v204
	v_lshl_or_b32 v2, s73, 8, v201
	v_cvt_pk_fp8_f32 v8, v12, v14 op_sel:[0,0,1]
	v_cvt_pk_fp8_f32 v9, v13, v5 op_sel:[0,0,1]
	v_ashrrev_i32_e32 v3, 31, v2
	v_lshl_add_u64 v[0:1], s[86:87], 0, v[0:1]
	v_lshl_add_u64 v[0:1], v[0:1], 0, v[2:3]
	s_mov_b32 s98, 0xffff0000
	s_mov_b32 s99, 0xffff0000
	v_mov_b32_e32 v178, 0x78
	v_mov_b32_e32 v179, 0
	v_permlane16_swap_b32_e32 v6, v8
	v_permlane16_swap_b32_e32 v7, v9
	v_cndmask_b32_e64 v178, 0, v178, s[98:99]
	v_cndmask_b32_e64 v176, v0, v0, s[98:99]
	v_cndmask_b32_e64 v177, v1, v1, s[98:99]
	v_lshl_add_u64 v[176:177], v[176:177], 0, v[178:179]
	global_store_dwordx4 v[176:177], v[6:9], off
	s_nop 1
	v_mul_f32_e32 v8, 0x3b800000, v136
	v_med3_f32 v10, v8, s72, v204
	v_mul_f32_e32 v8, 0x3b800000, v141
	v_med3_f32 v9, v8, s72, v204
	v_mul_f32_e32 v8, 0x3b800000, v137
	v_med3_f32 v11, v8, s72, v204
	v_mul_f32_e32 v8, 0x3b800000, v142
	v_med3_f32 v12, v8, s72, v204
	v_mul_f32_e32 v8, 0x3b800000, v138
	v_mul_f32_e32 v5, 0x3b800000, v140
	v_med3_f32 v13, v8, s72, v204
	v_mul_f32_e32 v8, 0x3b800000, v143
	v_med3_f32 v5, v5, s72, v204
	v_med3_f32 v14, v8, s72, v204
	v_mov_b32_e32 v8, 0
	v_cvt_pk_fp8_f32 v8, v5, v9
	v_mov_b32_e32 v9, 0
	v_cvt_pk_fp8_f32 v9, v10, v11
	v_mul_f32_e32 v10, 0x3b800000, v128
	v_mul_f32_e32 v5, 0x3b800000, v139
	v_cvt_pk_fp8_f32 v8, v12, v14 op_sel:[0,0,1]
	v_med3_f32 v12, v10, s72, v204
	v_mul_f32_e32 v10, 0x3b800000, v133
	v_med3_f32 v5, v5, s72, v204
	v_med3_f32 v11, v10, s72, v204
	v_mul_f32_e32 v10, 0x3b800000, v129
	v_cvt_pk_fp8_f32 v9, v13, v5 op_sel:[0,0,1]
	v_med3_f32 v13, v10, s72, v204
	v_mul_f32_e32 v10, 0x3b800000, v134
	v_med3_f32 v14, v10, s72, v204
	v_mul_f32_e32 v10, 0x3b800000, v130
	v_mul_f32_e32 v5, 0x3b800000, v132
	v_med3_f32 v15, v10, s72, v204
	v_mul_f32_e32 v10, 0x3b800000, v135
	v_med3_f32 v5, v5, s72, v204
	v_med3_f32 v16, v10, s72, v204
	v_mov_b32_e32 v10, 0
	v_cvt_pk_fp8_f32 v10, v5, v11
	v_mov_b32_e32 v11, 0
	v_cvt_pk_fp8_f32 v11, v12, v13
	v_or_b32_e32 v6, 16, v4
	v_mul_f32_e32 v5, 0x3b800000, v131
	v_ashrrev_i32_e32 v7, 31, v6
	v_med3_f32 v5, v5, s72, v204
	v_lshlrev_b64 v[6:7], 10, v[6:7]
	v_cvt_pk_fp8_f32 v10, v14, v16 op_sel:[0,0,1]
	v_cvt_pk_fp8_f32 v11, v15, v5 op_sel:[0,0,1]
	v_lshl_add_u64 v[6:7], s[86:87], 0, v[6:7]
	v_lshl_add_u64 v[6:7], v[6:7], 0, v[2:3]
	s_mov_b32 s98, 0xffff0000
	s_mov_b32 s99, 0xffff0000
	v_mov_b32_e32 v178, 0x78
	v_mov_b32_e32 v179, 0
	v_permlane16_swap_b32_e32 v8, v10
	v_permlane16_swap_b32_e32 v9, v11
	v_cndmask_b32_e64 v178, 0, v178, s[98:99]
	v_cndmask_b32_e64 v176, v6, v6, s[98:99]
	v_cndmask_b32_e64 v177, v7, v7, s[98:99]
	v_lshl_add_u64 v[176:177], v[176:177], 0, v[178:179]
	global_store_dwordx4 v[176:177], v[8:11], off
	s_nop 1
	v_mul_f32_e32 v8, 0x3b800000, v120
	v_med3_f32 v10, v8, s72, v204
	v_mul_f32_e32 v8, 0x3b800000, v125
	v_med3_f32 v9, v8, s72, v204
	v_mul_f32_e32 v8, 0x3b800000, v121
	v_med3_f32 v11, v8, s72, v204
	v_mul_f32_e32 v8, 0x3b800000, v126
	v_med3_f32 v12, v8, s72, v204
	v_mul_f32_e32 v8, 0x3b800000, v122
	v_mul_f32_e32 v5, 0x3b800000, v124
	v_med3_f32 v13, v8, s72, v204
	v_mul_f32_e32 v8, 0x3b800000, v127
	v_med3_f32 v5, v5, s72, v204
	v_med3_f32 v14, v8, s72, v204
	v_mov_b32_e32 v8, 0
	v_cvt_pk_fp8_f32 v8, v5, v9
	v_mov_b32_e32 v9, 0
	v_cvt_pk_fp8_f32 v9, v10, v11
	v_mul_f32_e32 v10, 0x3b800000, v112
	v_mul_f32_e32 v5, 0x3b800000, v123
	v_cvt_pk_fp8_f32 v8, v12, v14 op_sel:[0,0,1]
	v_med3_f32 v12, v10, s72, v204
	v_mul_f32_e32 v10, 0x3b800000, v117
	v_med3_f32 v5, v5, s72, v204
	v_med3_f32 v11, v10, s72, v204
	v_mul_f32_e32 v10, 0x3b800000, v113
	v_cvt_pk_fp8_f32 v9, v13, v5 op_sel:[0,0,1]
	v_med3_f32 v13, v10, s72, v204
	v_mul_f32_e32 v10, 0x3b800000, v118
	v_med3_f32 v14, v10, s72, v204
	v_mul_f32_e32 v10, 0x3b800000, v114
	v_mul_f32_e32 v5, 0x3b800000, v116
	v_med3_f32 v15, v10, s72, v204
	v_mul_f32_e32 v10, 0x3b800000, v119
	v_med3_f32 v5, v5, s72, v204
	v_med3_f32 v16, v10, s72, v204
	v_mov_b32_e32 v10, 0
	v_cvt_pk_fp8_f32 v10, v5, v11
	v_mov_b32_e32 v11, 0
	v_cvt_pk_fp8_f32 v11, v12, v13
	v_or_b32_e32 v6, 32, v4
	v_mul_f32_e32 v5, 0x3b800000, v115
	v_ashrrev_i32_e32 v7, 31, v6
	v_med3_f32 v5, v5, s72, v204
	v_lshlrev_b64 v[6:7], 10, v[6:7]
	v_cvt_pk_fp8_f32 v10, v14, v16 op_sel:[0,0,1]
	v_cvt_pk_fp8_f32 v11, v15, v5 op_sel:[0,0,1]
	v_lshl_add_u64 v[6:7], s[86:87], 0, v[6:7]
	v_lshl_add_u64 v[6:7], v[6:7], 0, v[2:3]
	s_mov_b32 s98, 0xffff0000
	s_mov_b32 s99, 0xffff0000
	v_mov_b32_e32 v178, 0x78
	v_mov_b32_e32 v179, 0
	v_permlane16_swap_b32_e32 v8, v10
	v_permlane16_swap_b32_e32 v9, v11
	v_cndmask_b32_e64 v178, 0, v178, s[98:99]
	v_cndmask_b32_e64 v176, v6, v6, s[98:99]
	v_cndmask_b32_e64 v177, v7, v7, s[98:99]
	v_lshl_add_u64 v[176:177], v[176:177], 0, v[178:179]
	global_store_dwordx4 v[176:177], v[8:11], off
	s_nop 1
	v_mul_f32_e32 v6, 0x3b800000, v108
	v_med3_f32 v7, v6, s72, v204
	v_mul_f32_e32 v6, 0x3b800000, v104
	v_med3_f32 v8, v6, s72, v204
	v_mul_f32_e32 v6, 0x3b800000, v109
	v_med3_f32 v9, v6, s72, v204
	v_mul_f32_e32 v6, 0x3b800000, v105
	v_med3_f32 v10, v6, s72, v204
	v_mul_f32_e32 v6, 0x3b800000, v110
	v_med3_f32 v11, v6, s72, v204
	v_mul_f32_e32 v6, 0x3b800000, v106
	v_med3_f32 v12, v6, s72, v204
	v_mul_f32_e32 v6, 0x3b800000, v111
	v_med3_f32 v13, v6, s72, v204
	v_mov_b32_e32 v6, 0
	v_cvt_pk_fp8_f32 v6, v7, v9
	v_mov_b32_e32 v7, 0
	v_cvt_pk_fp8_f32 v7, v8, v10
	v_mul_f32_e32 v8, 0x3b800000, v107
	v_med3_f32 v8, v8, s72, v204
	v_cvt_pk_fp8_f32 v6, v11, v13 op_sel:[0,0,1]
	v_cvt_pk_fp8_f32 v7, v12, v8 op_sel:[0,0,1]
	v_mul_f32_e32 v8, 0x3b800000, v92
	v_med3_f32 v9, v8, s72, v204
	v_mul_f32_e32 v8, 0x3b800000, v88
	v_med3_f32 v10, v8, s72, v204
	v_mul_f32_e32 v8, 0x3b800000, v93
	v_med3_f32 v11, v8, s72, v204
	v_mul_f32_e32 v8, 0x3b800000, v89
	v_med3_f32 v12, v8, s72, v204
	v_mul_f32_e32 v8, 0x3b800000, v94
	v_med3_f32 v13, v8, s72, v204
	v_mul_f32_e32 v8, 0x3b800000, v90
	v_med3_f32 v14, v8, s72, v204
	v_mul_f32_e32 v8, 0x3b800000, v95
	v_med3_f32 v15, v8, s72, v204
	v_mov_b32_e32 v8, 0
	v_cvt_pk_fp8_f32 v8, v9, v11
	v_mov_b32_e32 v9, 0
	v_cvt_pk_fp8_f32 v9, v10, v12
	v_or_b32_e32 v4, 48, v4
	v_ashrrev_i32_e32 v5, 31, v4
	v_mul_f32_e32 v10, 0x3b800000, v91
	v_lshlrev_b64 v[4:5], 10, v[4:5]
	v_med3_f32 v10, v10, s72, v204
	v_cvt_pk_fp8_f32 v8, v13, v15 op_sel:[0,0,1]
	v_cvt_pk_fp8_f32 v9, v14, v10 op_sel:[0,0,1]
	v_lshl_add_u64 v[4:5], s[86:87], 0, v[4:5]
	v_lshl_add_u64 v[2:3], v[4:5], 0, v[2:3]
	v_mul_f32_e32 v4, 0x3b800000, v84
	v_med3_f32 v5, v4, s72, v204
	v_mul_f32_e32 v4, 0x3b800000, v76
	s_mov_b32 s98, 0xffff0000
	s_mov_b32 s99, 0xffff0000
	v_mov_b32_e32 v178, 0x78
	v_mov_b32_e32 v179, 0
	v_permlane16_swap_b32_e32 v6, v8
	v_permlane16_swap_b32_e32 v7, v9
	v_cndmask_b32_e64 v178, 0, v178, s[98:99]
	v_cndmask_b32_e64 v176, v2, v2, s[98:99]
	v_cndmask_b32_e64 v177, v3, v3, s[98:99]
	v_lshl_add_u64 v[176:177], v[176:177], 0, v[178:179]
	global_store_dwordx4 v[176:177], v[6:9], off
	s_nop 1
	v_med3_f32 v6, v4, s72, v204
	v_mul_f32_e32 v4, 0x3b800000, v85
	v_med3_f32 v7, v4, s72, v204
	v_mul_f32_e32 v4, 0x3b800000, v77
	v_med3_f32 v8, v4, s72, v204
	v_mul_f32_e32 v4, 0x3b800000, v86
	v_med3_f32 v9, v4, s72, v204
	v_mul_f32_e32 v4, 0x3b800000, v78
	v_med3_f32 v10, v4, s72, v204
	v_mul_f32_e32 v4, 0x3b800000, v87
	v_med3_f32 v11, v4, s72, v204
	v_mov_b32_e32 v4, 0
	v_cvt_pk_fp8_f32 v4, v5, v7
	v_mov_b32_e32 v5, 0
	v_cvt_pk_fp8_f32 v5, v6, v8
	v_mul_f32_e32 v6, 0x3b800000, v79
	v_med3_f32 v6, v6, s72, v204
	v_cvt_pk_fp8_f32 v4, v9, v11 op_sel:[0,0,1]
	v_cvt_pk_fp8_f32 v5, v10, v6 op_sel:[0,0,1]
	v_mul_f32_e32 v6, 0x3b800000, v100
	v_med3_f32 v7, v6, s72, v204
	v_mul_f32_e32 v6, 0x3b800000, v96
	v_med3_f32 v8, v6, s72, v204
	v_mul_f32_e32 v6, 0x3b800000, v101
	v_med3_f32 v9, v6, s72, v204
	v_mul_f32_e32 v6, 0x3b800000, v97
	v_med3_f32 v10, v6, s72, v204
	v_mul_f32_e32 v6, 0x3b800000, v102
	v_med3_f32 v11, v6, s72, v204
	v_mul_f32_e32 v6, 0x3b800000, v98
	v_med3_f32 v12, v6, s72, v204
	v_mul_f32_e32 v6, 0x3b800000, v103
	v_med3_f32 v13, v6, s72, v204
	v_mov_b32_e32 v6, 0
	v_cvt_pk_fp8_f32 v6, v7, v9
	v_mov_b32_e32 v7, 0
	v_cvt_pk_fp8_f32 v7, v8, v10
	v_mul_f32_e32 v8, 0x3b800000, v99
	v_med3_f32 v8, v8, s72, v204
	v_cvt_pk_fp8_f32 v6, v11, v13 op_sel:[0,0,1]
	v_cvt_pk_fp8_f32 v7, v12, v8 op_sel:[0,0,1]
	s_mov_b32 s15, 0x20000
	v_add_co_u32_e32 v8, vcc, s15, v0
	s_mov_b64 s[22:23], 0x20000
	s_nop 0
	v_addc_co_u32_e32 v9, vcc, 0, v1, vcc
	v_lshl_add_u64 v[2:3], v[0:1], 0, s[22:23]
	s_mov_b32 s98, 0xffff0000
	s_mov_b32 s99, 0xffff0000
	v_mov_b32_e32 v178, 0x78
	v_mov_b32_e32 v179, 0
	v_permlane16_swap_b32_e32 v4, v6
	v_permlane16_swap_b32_e32 v5, v7
	v_cndmask_b32_e64 v178, 0, v178, s[98:99]
	v_cndmask_b32_e64 v176, v8, v2, s[98:99]
	v_cndmask_b32_e64 v177, v9, v3, s[98:99]
	v_lshl_add_u64 v[176:177], v[176:177], 0, v[178:179]
	global_store_dwordx4 v[176:177], v[4:7], off
	s_nop 1
	v_mul_f32_e32 v4, 0x3b800000, v60
	v_med3_f32 v5, v4, s72, v204
	v_mul_f32_e32 v4, 0x3b800000, v48
	v_med3_f32 v6, v4, s72, v204
	v_mul_f32_e32 v4, 0x3b800000, v61
	v_med3_f32 v7, v4, s72, v204
	v_mul_f32_e32 v4, 0x3b800000, v49
	v_med3_f32 v8, v4, s72, v204
	v_mul_f32_e32 v4, 0x3b800000, v62
	v_med3_f32 v9, v4, s72, v204
	v_mul_f32_e32 v4, 0x3b800000, v50
	v_med3_f32 v10, v4, s72, v204
	v_mul_f32_e32 v4, 0x3b800000, v63
	v_med3_f32 v11, v4, s72, v204
	v_mov_b32_e32 v4, 0
	v_cvt_pk_fp8_f32 v4, v5, v7
	v_mov_b32_e32 v5, 0
	v_cvt_pk_fp8_f32 v5, v6, v8
	v_mul_f32_e32 v6, 0x3b800000, v51
	v_med3_f32 v6, v6, s72, v204
	v_cvt_pk_fp8_f32 v4, v9, v11 op_sel:[0,0,1]
	v_cvt_pk_fp8_f32 v5, v10, v6 op_sel:[0,0,1]
	v_mul_f32_e32 v6, 0x3b800000, v80
	v_med3_f32 v7, v6, s72, v204
	v_mul_f32_e32 v6, 0x3b800000, v72
	v_med3_f32 v8, v6, s72, v204
	v_mul_f32_e32 v6, 0x3b800000, v81
	v_med3_f32 v9, v6, s72, v204
	v_mul_f32_e32 v6, 0x3b800000, v73
	v_med3_f32 v10, v6, s72, v204
	v_mul_f32_e32 v6, 0x3b800000, v82
	v_med3_f32 v11, v6, s72, v204
	v_mul_f32_e32 v6, 0x3b800000, v74
	v_med3_f32 v12, v6, s72, v204
	v_mul_f32_e32 v6, 0x3b800000, v83
	v_med3_f32 v13, v6, s72, v204
	v_mov_b32_e32 v6, 0
	v_cvt_pk_fp8_f32 v6, v7, v9
	v_mov_b32_e32 v7, 0
	v_cvt_pk_fp8_f32 v7, v8, v10
	v_mul_f32_e32 v8, 0x3b800000, v75
	v_med3_f32 v8, v8, s72, v204
	v_cvt_pk_fp8_f32 v6, v11, v13 op_sel:[0,0,1]
	v_cvt_pk_fp8_f32 v7, v12, v8 op_sel:[0,0,1]
	s_mov_b32 s15, 0x24000
	v_add_co_u32_e32 v8, vcc, s15, v0
	s_mov_b64 s[22:23], 0x24000
	s_nop 0
	v_addc_co_u32_e32 v9, vcc, 0, v1, vcc
	v_lshl_add_u64 v[2:3], v[0:1], 0, s[22:23]
	s_mov_b32 s98, 0xffff0000
	s_mov_b32 s99, 0xffff0000
	v_mov_b32_e32 v178, 0x78
	v_mov_b32_e32 v179, 0
	v_permlane16_swap_b32_e32 v4, v6
	v_permlane16_swap_b32_e32 v5, v7
	v_cndmask_b32_e64 v178, 0, v178, s[98:99]
	v_cndmask_b32_e64 v176, v8, v2, s[98:99]
	v_cndmask_b32_e64 v177, v9, v3, s[98:99]
	v_lshl_add_u64 v[176:177], v[176:177], 0, v[178:179]
	global_store_dwordx4 v[176:177], v[4:7], off
	s_nop 1
	v_mul_f32_e32 v4, 0x3b800000, v68
	v_med3_f32 v5, v4, s72, v204
	v_mul_f32_e32 v4, 0x3b800000, v56
	v_med3_f32 v6, v4, s72, v204
	v_mul_f32_e32 v4, 0x3b800000, v69
	v_med3_f32 v7, v4, s72, v204
	v_mul_f32_e32 v4, 0x3b800000, v57
	v_med3_f32 v8, v4, s72, v204
	v_mul_f32_e32 v4, 0x3b800000, v70
	v_med3_f32 v9, v4, s72, v204
	v_mul_f32_e32 v4, 0x3b800000, v58
	v_med3_f32 v10, v4, s72, v204
	v_mul_f32_e32 v4, 0x3b800000, v71
	v_med3_f32 v11, v4, s72, v204
	v_mov_b32_e32 v4, 0
	v_cvt_pk_fp8_f32 v4, v5, v7
	v_mov_b32_e32 v5, 0
	v_cvt_pk_fp8_f32 v5, v6, v8
	v_mul_f32_e32 v6, 0x3b800000, v59
	v_med3_f32 v6, v6, s72, v204
	v_cvt_pk_fp8_f32 v4, v9, v11 op_sel:[0,0,1]
	v_cvt_pk_fp8_f32 v5, v10, v6 op_sel:[0,0,1]
	v_mul_f32_e32 v6, 0x3b800000, v64
	v_med3_f32 v7, v6, s72, v204
	v_mul_f32_e32 v6, 0x3b800000, v52
	v_med3_f32 v8, v6, s72, v204
	v_mul_f32_e32 v6, 0x3b800000, v65
	v_med3_f32 v9, v6, s72, v204
	v_mul_f32_e32 v6, 0x3b800000, v53
	v_med3_f32 v10, v6, s72, v204
	v_mul_f32_e32 v6, 0x3b800000, v66
	v_med3_f32 v11, v6, s72, v204
	v_mul_f32_e32 v6, 0x3b800000, v54
	v_med3_f32 v12, v6, s72, v204
	v_mul_f32_e32 v6, 0x3b800000, v67
	v_med3_f32 v13, v6, s72, v204
	v_mov_b32_e32 v6, 0
	v_cvt_pk_fp8_f32 v6, v7, v9
	v_mov_b32_e32 v7, 0
	v_cvt_pk_fp8_f32 v7, v8, v10
	v_mul_f32_e32 v8, 0x3b800000, v55
	v_med3_f32 v8, v8, s72, v204
	v_cvt_pk_fp8_f32 v6, v11, v13 op_sel:[0,0,1]
	v_cvt_pk_fp8_f32 v7, v12, v8 op_sel:[0,0,1]
	s_mov_b32 s15, 0x28000
	v_add_co_u32_e32 v8, vcc, s15, v0
	s_mov_b64 s[22:23], 0x28000
	s_nop 0
	v_addc_co_u32_e32 v9, vcc, 0, v1, vcc
	v_lshl_add_u64 v[2:3], v[0:1], 0, s[22:23]
	s_mov_b32 s98, 0xffff0000
	s_mov_b32 s99, 0xffff0000
	v_mov_b32_e32 v178, 0x78
	v_mov_b32_e32 v179, 0
	v_permlane16_swap_b32_e32 v4, v6
	v_permlane16_swap_b32_e32 v5, v7
	v_cndmask_b32_e64 v178, 0, v178, s[98:99]
	v_cndmask_b32_e64 v176, v8, v2, s[98:99]
	v_cndmask_b32_e64 v177, v9, v3, s[98:99]
	v_lshl_add_u64 v[176:177], v[176:177], 0, v[178:179]
	global_store_dwordx4 v[176:177], v[4:7], off
	s_nop 1
	v_mul_f32_e32 v4, 0x3b800000, v44
	v_med3_f32 v5, v4, s72, v204
	v_mul_f32_e32 v4, 0x3b800000, v36
	v_med3_f32 v6, v4, s72, v204
	v_mul_f32_e32 v4, 0x3b800000, v45
	v_med3_f32 v7, v4, s72, v204
	v_mul_f32_e32 v4, 0x3b800000, v37
	v_med3_f32 v8, v4, s72, v204
	v_mul_f32_e32 v4, 0x3b800000, v46
	v_med3_f32 v9, v4, s72, v204
	v_mul_f32_e32 v4, 0x3b800000, v38
	v_med3_f32 v10, v4, s72, v204
	v_mul_f32_e32 v4, 0x3b800000, v47
	v_med3_f32 v11, v4, s72, v204
	v_mov_b32_e32 v4, 0
	v_cvt_pk_fp8_f32 v4, v5, v7
	v_mov_b32_e32 v5, 0
	v_cvt_pk_fp8_f32 v5, v6, v8
	v_mul_f32_e32 v6, 0x3b800000, v39
	v_med3_f32 v6, v6, s72, v204
	v_cvt_pk_fp8_f32 v4, v9, v11 op_sel:[0,0,1]
	v_cvt_pk_fp8_f32 v5, v10, v6 op_sel:[0,0,1]
	v_mul_f32_e32 v6, 0x3b800000, v40
	v_med3_f32 v7, v6, s72, v204
	v_mul_f32_e32 v6, 0x3b800000, v32
	v_med3_f32 v8, v6, s72, v204
	v_mul_f32_e32 v6, 0x3b800000, v41
	v_med3_f32 v9, v6, s72, v204
	v_mul_f32_e32 v6, 0x3b800000, v33
	v_med3_f32 v10, v6, s72, v204
	v_mul_f32_e32 v6, 0x3b800000, v42
	v_med3_f32 v11, v6, s72, v204
	v_mul_f32_e32 v6, 0x3b800000, v34
	v_med3_f32 v12, v6, s72, v204
	v_mul_f32_e32 v6, 0x3b800000, v43
	v_med3_f32 v13, v6, s72, v204
	v_mov_b32_e32 v6, 0
	v_cvt_pk_fp8_f32 v6, v7, v9
	v_mov_b32_e32 v7, 0
	v_cvt_pk_fp8_f32 v7, v8, v10
	v_mul_f32_e32 v8, 0x3b800000, v35
	s_mov_b64 s[22:23], 0x2c000
	v_med3_f32 v8, v8, s72, v204
	s_mov_b32 s15, 0x2c000
	v_lshl_add_u64 v[2:3], v[0:1], 0, s[22:23]
	v_cvt_pk_fp8_f32 v6, v11, v13 op_sel:[0,0,1]
	v_cvt_pk_fp8_f32 v7, v12, v8 op_sel:[0,0,1]
	v_add_co_u32_e32 v0, vcc, s15, v0
	v_readlane_b32 s74, v254, 58
	s_nop 0
	v_addc_co_u32_e32 v1, vcc, 0, v1, vcc
	s_andn2_b64 vcc, exec, s[4:5]
	s_mov_b64 s[4:5], -1
	s_mov_b32 s98, 0xffff0000
	s_mov_b32 s99, 0xffff0000
	v_mov_b32_e32 v178, 0x78
	v_mov_b32_e32 v179, 0
	v_permlane16_swap_b32_e32 v4, v6
	v_permlane16_swap_b32_e32 v5, v7
	v_cndmask_b32_e64 v178, 0, v178, s[98:99]
	v_cndmask_b32_e64 v176, v0, v2, s[98:99]
	v_cndmask_b32_e64 v177, v1, v3, s[98:99]
	v_lshl_add_u64 v[176:177], v[176:177], 0, v[178:179]
	global_store_dwordx4 v[176:177], v[4:7], off
	s_nop 1
	s_cbranch_vccnz .LBB0_3413
	s_andn2_b64 vcc, exec, s[6:7]
	s_cbranch_vccnz .LBB0_3412
	s_barrier
	s_branch .LBB0_3412
